# P11 tile loop: all eight KI fragment ds_reads issued up front into unused v228-v247 with counted lgkmcnt waits (30 of 32 unrolled tiles), on top of the top-256 fast path
# speedup vs baseline: 1.0174x; 1.0065x over previous
.LBB0_928:
	ds_read_b128 v[2:5], v1 offset:8192
	ds_read_b128 v[18:21], v1 offset:12288
	ds_read_b128 v[94:97], v67 offset:8192
	ds_read_b128 v[228:231], v67 offset:12288
	ds_read_b128 v[232:235], v69 offset:8192
	ds_read_b128 v[236:239], v69 offset:12288
	ds_read_b128 v[240:243], v92 offset:8192
	ds_read_b128 v[244:247], v92 offset:12288
	s_waitcnt lgkmcnt(5)
	v_mfma_f32_32x32x16_bf16 v[2:17], v[62:65], v[2:5], 0
	v_mfma_f32_32x32x16_bf16 v[18:33], v[62:65], v[18:21], 0
	v_mfma_f32_32x32x16_bf16 v[2:17], v[58:61], v[94:97], v[2:17]
	s_waitcnt lgkmcnt(4)
	v_mfma_f32_32x32x16_bf16 v[18:33], v[58:61], v[228:231], v[18:33]
	s_waitcnt lgkmcnt(3)
	v_mfma_f32_32x32x16_bf16 v[2:17], v[54:57], v[232:235], v[2:17]
	s_waitcnt lgkmcnt(2)
	v_mfma_f32_32x32x16_bf16 v[18:33], v[54:57], v[236:239], v[18:33]
	s_waitcnt lgkmcnt(1)
	v_mfma_f32_32x32x16_bf16 v[2:17], v[50:53], v[240:243], v[2:17]
	s_waitcnt lgkmcnt(0)
	v_mfma_f32_32x32x16_bf16 v[18:33], v[50:53], v[244:247], v[18:33]
	s_nop 9
	v_max_i32_e32 v98, 0, v2
	v_max_i32_e32 v96, 0, v10
	v_max_i32_e32 v2, 0, v3
	v_max_i32_e32 v10, 0, v11
	v_max_i32_e32 v99, 0, v18
	v_pk_fma_f32 v[94:95], v[74:75], v[98:99], 0 op_sel_hi:[1,1,0]
	v_max_i32_e32 v97, 0, v26
	v_max_i32_e32 v3, 0, v19
	v_pk_fma_f32 v[96:97], v[76:77], v[96:97], 0 op_sel_hi:[1,1,0]
	v_pk_fma_f32 v[2:3], v[46:47], v[2:3], v[94:95]
	v_max_i32_e32 v11, 0, v27
	v_max_i32_e32 v18, 0, v4
	v_max_i32_e32 v19, 0, v20
	v_pk_fma_f32 v[10:11], v[42:43], v[10:11], v[96:97]
	v_pk_fma_f32 v[2:3], v[78:79], v[18:19], v[2:3]
	v_max_i32_e32 v18, 0, v12
	v_max_i32_e32 v19, 0, v28
	v_max_i32_e32 v4, 0, v5
	v_max_i32_e32 v5, 0, v21
	v_pk_fma_f32 v[10:11], v[80:81], v[18:19], v[10:11]
	v_pk_fma_f32 v[2:3], v[48:49], v[4:5], v[2:3]
	v_max_i32_e32 v4, 0, v13
	v_max_i32_e32 v5, 0, v29
	v_pk_fma_f32 v[4:5], v[44:45], v[4:5], v[10:11]
	v_max_i32_e32 v10, 0, v6
	v_max_i32_e32 v11, 0, v22
	v_pk_fma_f32 v[2:3], v[82:83], v[10:11], v[2:3]
	v_max_i32_e32 v10, 0, v14
	v_max_i32_e32 v11, 0, v30
	v_max_i32_e32 v6, 0, v7
	v_max_i32_e32 v7, 0, v23
	v_pk_fma_f32 v[4:5], v[84:85], v[10:11], v[4:5]
	v_pk_fma_f32 v[2:3], v[38:39], v[6:7], v[2:3]
	v_max_i32_e32 v6, 0, v15
	v_max_i32_e32 v7, 0, v31
	v_pk_fma_f32 v[4:5], v[34:35], v[6:7], v[4:5]
	v_max_i32_e32 v6, 0, v8
	v_max_i32_e32 v7, 0, v24
	v_pk_fma_f32 v[2:3], v[86:87], v[6:7], v[2:3]
	v_max_i32_e32 v6, 0, v16
	v_max_i32_e32 v7, 0, v32
	v_pk_fma_f32 v[4:5], v[88:89], v[6:7], v[4:5]
	v_max_i32_e32 v6, 0, v9
	v_max_i32_e32 v7, 0, v25
	v_pk_fma_f32 v[2:3], v[40:41], v[6:7], v[2:3]
	v_max_i32_e32 v6, 0, v17
	v_max_i32_e32 v7, 0, v33
	v_pk_fma_f32 v[4:5], v[36:37], v[6:7], v[4:5]
	v_not_b32_e32 v6, v2
	v_or_b32_e32 v7, 0x80000000, v2
	v_cmp_gt_i32_e32 vcc, 0, v2
	v_not_b32_e32 v2, v3
	s_nop 0
	v_cndmask_b32_e32 v179, v7, v6, vcc
	v_or_b32_e32 v6, 0x80000000, v3
	v_cmp_gt_i32_e32 vcc, 0, v3
	v_or_b32_e32 v3, 0x80000000, v4
	s_nop 0
	v_cndmask_b32_e32 v113, v6, v2, vcc
	v_not_b32_e32 v2, v4
	v_cmp_gt_i32_e32 vcc, 0, v4
	v_permlane32_swap_b32_e32 v179, v113
	s_nop 0
	v_cndmask_b32_e32 v142, v3, v2, vcc
	v_not_b32_e32 v2, v5
	v_or_b32_e32 v3, 0x80000000, v5
	v_cmp_gt_i32_e32 vcc, 0, v5
	s_nop 1
	v_cndmask_b32_e32 v94, v3, v2, vcc
	s_nop 1
	v_permlane32_swap_b32_e32 v142, v94

.LBB0_954:
	ds_read_b128 v[2:5], v1 offset:16384
	ds_read_b128 v[18:21], v1 offset:20480
	ds_read_b128 v[96:99], v67 offset:16384
	ds_read_b128 v[228:231], v67 offset:20480
	ds_read_b128 v[232:235], v69 offset:16384
	ds_read_b128 v[236:239], v69 offset:20480
	ds_read_b128 v[240:243], v92 offset:16384
	ds_read_b128 v[244:247], v92 offset:20480
	s_waitcnt lgkmcnt(5)
	v_mfma_f32_32x32x16_bf16 v[2:17], v[62:65], v[2:5], 0
	v_mfma_f32_32x32x16_bf16 v[18:33], v[62:65], v[18:21], 0
	v_mfma_f32_32x32x16_bf16 v[2:17], v[58:61], v[96:99], v[2:17]
	s_waitcnt lgkmcnt(4)
	v_mfma_f32_32x32x16_bf16 v[18:33], v[58:61], v[228:231], v[18:33]
	s_waitcnt lgkmcnt(3)
	v_mfma_f32_32x32x16_bf16 v[2:17], v[54:57], v[232:235], v[2:17]
	s_waitcnt lgkmcnt(2)
	v_mfma_f32_32x32x16_bf16 v[18:33], v[54:57], v[236:239], v[18:33]
	s_waitcnt lgkmcnt(1)
	v_mfma_f32_32x32x16_bf16 v[2:17], v[50:53], v[240:243], v[2:17]
	s_waitcnt lgkmcnt(0)
	v_mfma_f32_32x32x16_bf16 v[18:33], v[50:53], v[244:247], v[18:33]
	s_nop 9
	v_max_i32_e32 v100, 0, v2
	v_max_i32_e32 v98, 0, v10
	v_max_i32_e32 v2, 0, v3
	v_max_i32_e32 v10, 0, v11
	v_max_i32_e32 v101, 0, v18
	v_pk_fma_f32 v[96:97], v[74:75], v[100:101], 0 op_sel_hi:[1,1,0]
	v_max_i32_e32 v99, 0, v26
	v_max_i32_e32 v3, 0, v19
	v_pk_fma_f32 v[98:99], v[76:77], v[98:99], 0 op_sel_hi:[1,1,0]
	v_pk_fma_f32 v[2:3], v[46:47], v[2:3], v[96:97]
	v_max_i32_e32 v11, 0, v27
	v_max_i32_e32 v18, 0, v4
	v_max_i32_e32 v19, 0, v20
	v_pk_fma_f32 v[10:11], v[42:43], v[10:11], v[98:99]
	v_pk_fma_f32 v[2:3], v[78:79], v[18:19], v[2:3]
	v_max_i32_e32 v18, 0, v12
	v_max_i32_e32 v19, 0, v28
	v_max_i32_e32 v4, 0, v5
	v_max_i32_e32 v5, 0, v21
	v_pk_fma_f32 v[10:11], v[80:81], v[18:19], v[10:11]
	v_pk_fma_f32 v[2:3], v[48:49], v[4:5], v[2:3]
	v_max_i32_e32 v4, 0, v13
	v_max_i32_e32 v5, 0, v29
	v_pk_fma_f32 v[4:5], v[44:45], v[4:5], v[10:11]
	v_max_i32_e32 v10, 0, v6
	v_max_i32_e32 v11, 0, v22
	v_pk_fma_f32 v[2:3], v[82:83], v[10:11], v[2:3]
	v_max_i32_e32 v10, 0, v14
	v_max_i32_e32 v11, 0, v30
	v_max_i32_e32 v6, 0, v7
	v_max_i32_e32 v7, 0, v23
	v_pk_fma_f32 v[4:5], v[84:85], v[10:11], v[4:5]
	v_pk_fma_f32 v[2:3], v[38:39], v[6:7], v[2:3]
	v_max_i32_e32 v6, 0, v15
	v_max_i32_e32 v7, 0, v31
	v_pk_fma_f32 v[4:5], v[34:35], v[6:7], v[4:5]
	v_max_i32_e32 v6, 0, v8
	v_max_i32_e32 v7, 0, v24
	v_pk_fma_f32 v[2:3], v[86:87], v[6:7], v[2:3]
	v_max_i32_e32 v6, 0, v16
	v_max_i32_e32 v7, 0, v32
	v_pk_fma_f32 v[4:5], v[88:89], v[6:7], v[4:5]
	v_max_i32_e32 v6, 0, v9
	v_max_i32_e32 v7, 0, v25
	v_pk_fma_f32 v[2:3], v[40:41], v[6:7], v[2:3]
	v_max_i32_e32 v6, 0, v17
	v_max_i32_e32 v7, 0, v33
	v_pk_fma_f32 v[4:5], v[36:37], v[6:7], v[4:5]
	v_not_b32_e32 v6, v2
	v_or_b32_e32 v7, 0x80000000, v2
	v_cmp_gt_i32_e32 vcc, 0, v2
	v_not_b32_e32 v2, v3
	s_nop 0
	v_cndmask_b32_e32 v181, v7, v6, vcc
	v_or_b32_e32 v6, 0x80000000, v3
	v_cmp_gt_i32_e32 vcc, 0, v3
	v_or_b32_e32 v3, 0x80000000, v4
	s_nop 0
	v_cndmask_b32_e32 v115, v6, v2, vcc
	v_not_b32_e32 v2, v4
	v_cmp_gt_i32_e32 vcc, 0, v4
	v_permlane32_swap_b32_e32 v181, v115
	s_nop 0
	v_cndmask_b32_e32 v144, v3, v2, vcc
	v_not_b32_e32 v2, v5
	v_or_b32_e32 v3, 0x80000000, v5
	v_cmp_gt_i32_e32 vcc, 0, v5
	s_nop 1
	v_cndmask_b32_e32 v95, v3, v2, vcc
	s_nop 1
	v_permlane32_swap_b32_e32 v144, v95

.LBB0_980:
	ds_read_b128 v[2:5], v1 offset:24576
	ds_read_b128 v[18:21], v1 offset:28672
	ds_read_b128 v[96:99], v67 offset:24576
	ds_read_b128 v[228:231], v67 offset:28672
	ds_read_b128 v[232:235], v69 offset:24576
	ds_read_b128 v[236:239], v69 offset:28672
	ds_read_b128 v[240:243], v92 offset:24576
	ds_read_b128 v[244:247], v92 offset:28672
	s_waitcnt lgkmcnt(5)
	v_mfma_f32_32x32x16_bf16 v[2:17], v[62:65], v[2:5], 0
	v_mfma_f32_32x32x16_bf16 v[18:33], v[62:65], v[18:21], 0
	v_mfma_f32_32x32x16_bf16 v[2:17], v[58:61], v[96:99], v[2:17]
	s_waitcnt lgkmcnt(4)
	v_mfma_f32_32x32x16_bf16 v[18:33], v[58:61], v[228:231], v[18:33]
	s_waitcnt lgkmcnt(3)
	v_mfma_f32_32x32x16_bf16 v[2:17], v[54:57], v[232:235], v[2:17]
	s_waitcnt lgkmcnt(2)
	v_mfma_f32_32x32x16_bf16 v[18:33], v[54:57], v[236:239], v[18:33]
	s_waitcnt lgkmcnt(1)
	v_mfma_f32_32x32x16_bf16 v[2:17], v[50:53], v[240:243], v[2:17]
	s_waitcnt lgkmcnt(0)
	v_mfma_f32_32x32x16_bf16 v[18:33], v[50:53], v[244:247], v[18:33]
	s_nop 9
	v_max_i32_e32 v100, 0, v2
	v_max_i32_e32 v98, 0, v10
	v_max_i32_e32 v2, 0, v3
	v_max_i32_e32 v10, 0, v11
	v_max_i32_e32 v101, 0, v18
	v_pk_fma_f32 v[96:97], v[74:75], v[100:101], 0 op_sel_hi:[1,1,0]
	v_max_i32_e32 v99, 0, v26
	v_max_i32_e32 v3, 0, v19
	v_pk_fma_f32 v[98:99], v[76:77], v[98:99], 0 op_sel_hi:[1,1,0]
	v_pk_fma_f32 v[2:3], v[46:47], v[2:3], v[96:97]
	v_max_i32_e32 v11, 0, v27
	v_max_i32_e32 v18, 0, v4
	v_max_i32_e32 v19, 0, v20
	v_pk_fma_f32 v[10:11], v[42:43], v[10:11], v[98:99]
	v_pk_fma_f32 v[2:3], v[78:79], v[18:19], v[2:3]
	v_max_i32_e32 v18, 0, v12
	v_max_i32_e32 v19, 0, v28
	v_max_i32_e32 v4, 0, v5
	v_max_i32_e32 v5, 0, v21
	v_pk_fma_f32 v[10:11], v[80:81], v[18:19], v[10:11]
	v_pk_fma_f32 v[2:3], v[48:49], v[4:5], v[2:3]
	v_max_i32_e32 v4, 0, v13
	v_max_i32_e32 v5, 0, v29
	v_pk_fma_f32 v[4:5], v[44:45], v[4:5], v[10:11]
	v_max_i32_e32 v10, 0, v6
	v_max_i32_e32 v11, 0, v22
	v_pk_fma_f32 v[2:3], v[82:83], v[10:11], v[2:3]
	v_max_i32_e32 v10, 0, v14
	v_max_i32_e32 v11, 0, v30
	v_max_i32_e32 v6, 0, v7
	v_max_i32_e32 v7, 0, v23
	v_pk_fma_f32 v[4:5], v[84:85], v[10:11], v[4:5]
	v_pk_fma_f32 v[2:3], v[38:39], v[6:7], v[2:3]
	v_max_i32_e32 v6, 0, v15
	v_max_i32_e32 v7, 0, v31
	v_pk_fma_f32 v[4:5], v[34:35], v[6:7], v[4:5]
	v_max_i32_e32 v6, 0, v8
	v_max_i32_e32 v7, 0, v24
	v_pk_fma_f32 v[2:3], v[86:87], v[6:7], v[2:3]
	v_max_i32_e32 v6, 0, v16
	v_max_i32_e32 v7, 0, v32
	v_pk_fma_f32 v[4:5], v[88:89], v[6:7], v[4:5]
	v_max_i32_e32 v6, 0, v9
	v_max_i32_e32 v7, 0, v25
	v_pk_fma_f32 v[2:3], v[40:41], v[6:7], v[2:3]
	v_max_i32_e32 v6, 0, v17
	v_max_i32_e32 v7, 0, v33
	v_pk_fma_f32 v[4:5], v[36:37], v[6:7], v[4:5]
	v_not_b32_e32 v6, v2
	v_or_b32_e32 v7, 0x80000000, v2
	v_cmp_gt_i32_e32 vcc, 0, v2
	v_not_b32_e32 v2, v3
	s_nop 0
	v_cndmask_b32_e32 v183, v7, v6, vcc
	v_or_b32_e32 v6, 0x80000000, v3
	v_cmp_gt_i32_e32 vcc, 0, v3
	v_or_b32_e32 v3, 0x80000000, v4
	s_nop 0
	v_cndmask_b32_e32 v117, v6, v2, vcc
	v_not_b32_e32 v2, v4
	v_cmp_gt_i32_e32 vcc, 0, v4
	v_permlane32_swap_b32_e32 v183, v117
	s_nop 0
	v_cndmask_b32_e32 v146, v3, v2, vcc
	v_not_b32_e32 v2, v5
	v_or_b32_e32 v3, 0x80000000, v5
	v_cmp_gt_i32_e32 vcc, 0, v5
	s_nop 1
	v_cndmask_b32_e32 v96, v3, v2, vcc
	s_nop 1
	v_permlane32_swap_b32_e32 v146, v96

.LBB0_1006:
	ds_read_b128 v[2:5], v1 offset:32768
	ds_read_b128 v[18:21], v1 offset:36864
	ds_read_b128 v[98:101], v67 offset:32768
	ds_read_b128 v[228:231], v67 offset:36864
	ds_read_b128 v[232:235], v69 offset:32768
	ds_read_b128 v[236:239], v69 offset:36864
	ds_read_b128 v[240:243], v92 offset:32768
	ds_read_b128 v[244:247], v92 offset:36864
	s_waitcnt lgkmcnt(5)
	v_mfma_f32_32x32x16_bf16 v[2:17], v[62:65], v[2:5], 0
	v_mfma_f32_32x32x16_bf16 v[18:33], v[62:65], v[18:21], 0
	v_mfma_f32_32x32x16_bf16 v[2:17], v[58:61], v[98:101], v[2:17]
	s_waitcnt lgkmcnt(4)
	v_mfma_f32_32x32x16_bf16 v[18:33], v[58:61], v[228:231], v[18:33]
	s_waitcnt lgkmcnt(3)
	v_mfma_f32_32x32x16_bf16 v[2:17], v[54:57], v[232:235], v[2:17]
	s_waitcnt lgkmcnt(2)
	v_mfma_f32_32x32x16_bf16 v[18:33], v[54:57], v[236:239], v[18:33]
	s_waitcnt lgkmcnt(1)
	v_mfma_f32_32x32x16_bf16 v[2:17], v[50:53], v[240:243], v[2:17]
	s_waitcnt lgkmcnt(0)
	v_mfma_f32_32x32x16_bf16 v[18:33], v[50:53], v[244:247], v[18:33]
	s_nop 9
	v_max_i32_e32 v102, 0, v2
	v_max_i32_e32 v100, 0, v10
	v_max_i32_e32 v2, 0, v3
	v_max_i32_e32 v10, 0, v11
	v_max_i32_e32 v103, 0, v18
	v_pk_fma_f32 v[98:99], v[74:75], v[102:103], 0 op_sel_hi:[1,1,0]
	v_max_i32_e32 v101, 0, v26
	v_max_i32_e32 v3, 0, v19
	v_pk_fma_f32 v[100:101], v[76:77], v[100:101], 0 op_sel_hi:[1,1,0]
	v_pk_fma_f32 v[2:3], v[46:47], v[2:3], v[98:99]
	v_max_i32_e32 v11, 0, v27
	v_max_i32_e32 v18, 0, v4
	v_max_i32_e32 v19, 0, v20
	v_pk_fma_f32 v[10:11], v[42:43], v[10:11], v[100:101]
	v_pk_fma_f32 v[2:3], v[78:79], v[18:19], v[2:3]
	v_max_i32_e32 v18, 0, v12
	v_max_i32_e32 v19, 0, v28
	v_max_i32_e32 v4, 0, v5
	v_max_i32_e32 v5, 0, v21
	v_pk_fma_f32 v[10:11], v[80:81], v[18:19], v[10:11]
	v_pk_fma_f32 v[2:3], v[48:49], v[4:5], v[2:3]
	v_max_i32_e32 v4, 0, v13
	v_max_i32_e32 v5, 0, v29
	v_pk_fma_f32 v[4:5], v[44:45], v[4:5], v[10:11]
	v_max_i32_e32 v10, 0, v6
	v_max_i32_e32 v11, 0, v22
	v_pk_fma_f32 v[2:3], v[82:83], v[10:11], v[2:3]
	v_max_i32_e32 v10, 0, v14
	v_max_i32_e32 v11, 0, v30
	v_max_i32_e32 v6, 0, v7
	v_max_i32_e32 v7, 0, v23
	v_pk_fma_f32 v[4:5], v[84:85], v[10:11], v[4:5]
	v_pk_fma_f32 v[2:3], v[38:39], v[6:7], v[2:3]
	v_max_i32_e32 v6, 0, v15
	v_max_i32_e32 v7, 0, v31
	v_pk_fma_f32 v[4:5], v[34:35], v[6:7], v[4:5]
	v_max_i32_e32 v6, 0, v8
	v_max_i32_e32 v7, 0, v24
	v_pk_fma_f32 v[2:3], v[86:87], v[6:7], v[2:3]
	v_max_i32_e32 v6, 0, v16
	v_max_i32_e32 v7, 0, v32
	v_pk_fma_f32 v[4:5], v[88:89], v[6:7], v[4:5]
	v_max_i32_e32 v6, 0, v9
	v_max_i32_e32 v7, 0, v25
	v_pk_fma_f32 v[2:3], v[40:41], v[6:7], v[2:3]
	v_max_i32_e32 v6, 0, v17
	v_max_i32_e32 v7, 0, v33
	v_pk_fma_f32 v[4:5], v[36:37], v[6:7], v[4:5]
	v_not_b32_e32 v6, v2
	v_or_b32_e32 v7, 0x80000000, v2
	v_cmp_gt_i32_e32 vcc, 0, v2
	v_not_b32_e32 v2, v3
	s_nop 0
	v_cndmask_b32_e32 v185, v7, v6, vcc
	v_or_b32_e32 v6, 0x80000000, v3
	v_cmp_gt_i32_e32 vcc, 0, v3
	v_or_b32_e32 v3, 0x80000000, v4
	s_nop 0
	v_cndmask_b32_e32 v119, v6, v2, vcc
	v_not_b32_e32 v2, v4
	v_cmp_gt_i32_e32 vcc, 0, v4
	v_permlane32_swap_b32_e32 v185, v119
	s_nop 0
	v_cndmask_b32_e32 v148, v3, v2, vcc
	v_not_b32_e32 v2, v5
	v_or_b32_e32 v3, 0x80000000, v5
	v_cmp_gt_i32_e32 vcc, 0, v5
	s_nop 1
	v_cndmask_b32_e32 v97, v3, v2, vcc
	s_nop 1
	v_permlane32_swap_b32_e32 v148, v97

.LBB0_1032:
	ds_read_b128 v[2:5], v1 offset:40960
	ds_read_b128 v[18:21], v1 offset:45056
	ds_read_b128 v[98:101], v67 offset:40960
	ds_read_b128 v[228:231], v67 offset:45056
	ds_read_b128 v[232:235], v69 offset:40960
	ds_read_b128 v[236:239], v69 offset:45056
	ds_read_b128 v[240:243], v92 offset:40960
	ds_read_b128 v[244:247], v92 offset:45056
	s_waitcnt lgkmcnt(5)
	v_mfma_f32_32x32x16_bf16 v[2:17], v[62:65], v[2:5], 0
	v_mfma_f32_32x32x16_bf16 v[18:33], v[62:65], v[18:21], 0
	v_mfma_f32_32x32x16_bf16 v[2:17], v[58:61], v[98:101], v[2:17]
	s_waitcnt lgkmcnt(4)
	v_mfma_f32_32x32x16_bf16 v[18:33], v[58:61], v[228:231], v[18:33]
	s_waitcnt lgkmcnt(3)
	v_mfma_f32_32x32x16_bf16 v[2:17], v[54:57], v[232:235], v[2:17]
	s_waitcnt lgkmcnt(2)
	v_mfma_f32_32x32x16_bf16 v[18:33], v[54:57], v[236:239], v[18:33]
	s_waitcnt lgkmcnt(1)
	v_mfma_f32_32x32x16_bf16 v[2:17], v[50:53], v[240:243], v[2:17]
	s_waitcnt lgkmcnt(0)
	v_mfma_f32_32x32x16_bf16 v[18:33], v[50:53], v[244:247], v[18:33]
	s_nop 9
	v_max_i32_e32 v102, 0, v2
	v_max_i32_e32 v100, 0, v10
	v_max_i32_e32 v2, 0, v3
	v_max_i32_e32 v10, 0, v11
	v_max_i32_e32 v103, 0, v18
	v_pk_fma_f32 v[98:99], v[74:75], v[102:103], 0 op_sel_hi:[1,1,0]
	v_max_i32_e32 v101, 0, v26
	v_max_i32_e32 v3, 0, v19
	v_pk_fma_f32 v[100:101], v[76:77], v[100:101], 0 op_sel_hi:[1,1,0]
	v_pk_fma_f32 v[2:3], v[46:47], v[2:3], v[98:99]
	v_max_i32_e32 v11, 0, v27
	v_max_i32_e32 v18, 0, v4
	v_max_i32_e32 v19, 0, v20
	v_pk_fma_f32 v[10:11], v[42:43], v[10:11], v[100:101]
	v_pk_fma_f32 v[2:3], v[78:79], v[18:19], v[2:3]
	v_max_i32_e32 v18, 0, v12
	v_max_i32_e32 v19, 0, v28
	v_max_i32_e32 v4, 0, v5
	v_max_i32_e32 v5, 0, v21
	v_pk_fma_f32 v[10:11], v[80:81], v[18:19], v[10:11]
	v_pk_fma_f32 v[2:3], v[48:49], v[4:5], v[2:3]
	v_max_i32_e32 v4, 0, v13
	v_max_i32_e32 v5, 0, v29
	v_pk_fma_f32 v[4:5], v[44:45], v[4:5], v[10:11]
	v_max_i32_e32 v10, 0, v6
	v_max_i32_e32 v11, 0, v22
	v_pk_fma_f32 v[2:3], v[82:83], v[10:11], v[2:3]
	v_max_i32_e32 v10, 0, v14
	v_max_i32_e32 v11, 0, v30
	v_max_i32_e32 v6, 0, v7
	v_max_i32_e32 v7, 0, v23
	v_pk_fma_f32 v[4:5], v[84:85], v[10:11], v[4:5]
	v_pk_fma_f32 v[2:3], v[38:39], v[6:7], v[2:3]
	v_max_i32_e32 v6, 0, v15
	v_max_i32_e32 v7, 0, v31
	v_pk_fma_f32 v[4:5], v[34:35], v[6:7], v[4:5]
	v_max_i32_e32 v6, 0, v8
	v_max_i32_e32 v7, 0, v24
	v_pk_fma_f32 v[2:3], v[86:87], v[6:7], v[2:3]
	v_max_i32_e32 v6, 0, v16
	v_max_i32_e32 v7, 0, v32
	v_pk_fma_f32 v[4:5], v[88:89], v[6:7], v[4:5]
	v_max_i32_e32 v6, 0, v9
	v_max_i32_e32 v7, 0, v25
	v_pk_fma_f32 v[2:3], v[40:41], v[6:7], v[2:3]
	v_max_i32_e32 v6, 0, v17
	v_max_i32_e32 v7, 0, v33
	v_pk_fma_f32 v[4:5], v[36:37], v[6:7], v[4:5]
	v_not_b32_e32 v6, v2
	v_or_b32_e32 v7, 0x80000000, v2
	v_cmp_gt_i32_e32 vcc, 0, v2
	v_not_b32_e32 v2, v3
	s_nop 0
	v_cndmask_b32_e32 v187, v7, v6, vcc
	v_or_b32_e32 v6, 0x80000000, v3
	v_cmp_gt_i32_e32 vcc, 0, v3
	v_or_b32_e32 v3, 0x80000000, v4
	s_nop 0
	v_cndmask_b32_e32 v121, v6, v2, vcc
	v_not_b32_e32 v2, v4
	v_cmp_gt_i32_e32 vcc, 0, v4
	v_permlane32_swap_b32_e32 v187, v121
	s_nop 0
	v_cndmask_b32_e32 v150, v3, v2, vcc
	v_not_b32_e32 v2, v5
	v_or_b32_e32 v3, 0x80000000, v5
	v_cmp_gt_i32_e32 vcc, 0, v5
	s_nop 1
	v_cndmask_b32_e32 v98, v3, v2, vcc
	s_nop 1
	v_permlane32_swap_b32_e32 v150, v98

.LBB0_1058:
	ds_read_b128 v[2:5], v1 offset:49152
	ds_read_b128 v[18:21], v1 offset:53248
	ds_read_b128 v[100:103], v67 offset:49152
	ds_read_b128 v[228:231], v67 offset:53248
	ds_read_b128 v[232:235], v69 offset:49152
	ds_read_b128 v[236:239], v69 offset:53248
	ds_read_b128 v[240:243], v92 offset:49152
	ds_read_b128 v[244:247], v92 offset:53248
	s_waitcnt lgkmcnt(5)
	v_mfma_f32_32x32x16_bf16 v[2:17], v[62:65], v[2:5], 0
	v_mfma_f32_32x32x16_bf16 v[18:33], v[62:65], v[18:21], 0
	v_mfma_f32_32x32x16_bf16 v[2:17], v[58:61], v[100:103], v[2:17]
	s_waitcnt lgkmcnt(4)
	v_mfma_f32_32x32x16_bf16 v[18:33], v[58:61], v[228:231], v[18:33]
	s_waitcnt lgkmcnt(3)
	v_mfma_f32_32x32x16_bf16 v[2:17], v[54:57], v[232:235], v[2:17]
	s_waitcnt lgkmcnt(2)
	v_mfma_f32_32x32x16_bf16 v[18:33], v[54:57], v[236:239], v[18:33]
	s_waitcnt lgkmcnt(1)
	v_mfma_f32_32x32x16_bf16 v[2:17], v[50:53], v[240:243], v[2:17]
	s_waitcnt lgkmcnt(0)
	v_mfma_f32_32x32x16_bf16 v[18:33], v[50:53], v[244:247], v[18:33]
	s_nop 9
	v_max_i32_e32 v104, 0, v2
	v_max_i32_e32 v102, 0, v10
	v_max_i32_e32 v2, 0, v3
	v_max_i32_e32 v10, 0, v11
	v_max_i32_e32 v105, 0, v18
	v_pk_fma_f32 v[100:101], v[74:75], v[104:105], 0 op_sel_hi:[1,1,0]
	v_max_i32_e32 v103, 0, v26
	v_max_i32_e32 v3, 0, v19
	v_pk_fma_f32 v[102:103], v[76:77], v[102:103], 0 op_sel_hi:[1,1,0]
	v_pk_fma_f32 v[2:3], v[46:47], v[2:3], v[100:101]
	v_max_i32_e32 v11, 0, v27
	v_max_i32_e32 v18, 0, v4
	v_max_i32_e32 v19, 0, v20
	v_pk_fma_f32 v[10:11], v[42:43], v[10:11], v[102:103]
	v_pk_fma_f32 v[2:3], v[78:79], v[18:19], v[2:3]
	v_max_i32_e32 v18, 0, v12
	v_max_i32_e32 v19, 0, v28
	v_max_i32_e32 v4, 0, v5
	v_max_i32_e32 v5, 0, v21
	v_pk_fma_f32 v[10:11], v[80:81], v[18:19], v[10:11]
	v_pk_fma_f32 v[2:3], v[48:49], v[4:5], v[2:3]
	v_max_i32_e32 v4, 0, v13
	v_max_i32_e32 v5, 0, v29
	v_pk_fma_f32 v[4:5], v[44:45], v[4:5], v[10:11]
	v_max_i32_e32 v10, 0, v6
	v_max_i32_e32 v11, 0, v22
	v_pk_fma_f32 v[2:3], v[82:83], v[10:11], v[2:3]
	v_max_i32_e32 v10, 0, v14
	v_max_i32_e32 v11, 0, v30
	v_max_i32_e32 v6, 0, v7
	v_max_i32_e32 v7, 0, v23
	v_pk_fma_f32 v[4:5], v[84:85], v[10:11], v[4:5]
	v_pk_fma_f32 v[2:3], v[38:39], v[6:7], v[2:3]
	v_max_i32_e32 v6, 0, v15
	v_max_i32_e32 v7, 0, v31
	v_pk_fma_f32 v[4:5], v[34:35], v[6:7], v[4:5]
	v_max_i32_e32 v6, 0, v8
	v_max_i32_e32 v7, 0, v24
	v_pk_fma_f32 v[2:3], v[86:87], v[6:7], v[2:3]
	v_max_i32_e32 v6, 0, v16
	v_max_i32_e32 v7, 0, v32
	v_pk_fma_f32 v[4:5], v[88:89], v[6:7], v[4:5]
	v_max_i32_e32 v6, 0, v9
	v_max_i32_e32 v7, 0, v25
	v_pk_fma_f32 v[2:3], v[40:41], v[6:7], v[2:3]
	v_max_i32_e32 v6, 0, v17
	v_max_i32_e32 v7, 0, v33
	v_pk_fma_f32 v[4:5], v[36:37], v[6:7], v[4:5]
	v_not_b32_e32 v6, v2
	v_or_b32_e32 v7, 0x80000000, v2
	v_cmp_gt_i32_e32 vcc, 0, v2
	v_not_b32_e32 v2, v3
	s_nop 0
	v_cndmask_b32_e32 v189, v7, v6, vcc
	v_or_b32_e32 v6, 0x80000000, v3
	v_cmp_gt_i32_e32 vcc, 0, v3
	v_or_b32_e32 v3, 0x80000000, v4
	s_nop 0
	v_cndmask_b32_e32 v123, v6, v2, vcc
	v_not_b32_e32 v2, v4
	v_cmp_gt_i32_e32 vcc, 0, v4
	v_permlane32_swap_b32_e32 v189, v123
	s_nop 0
	v_cndmask_b32_e32 v152, v3, v2, vcc
	v_not_b32_e32 v2, v5
	v_or_b32_e32 v3, 0x80000000, v5
	v_cmp_gt_i32_e32 vcc, 0, v5
	s_nop 1
	v_cndmask_b32_e32 v99, v3, v2, vcc
	s_nop 1
	v_permlane32_swap_b32_e32 v152, v99

.LBB0_1084:
	ds_read_b128 v[2:5], v1 offset:57344
	ds_read_b128 v[18:21], v1 offset:61440
	ds_read_b128 v[100:103], v67 offset:57344
	ds_read_b128 v[228:231], v67 offset:61440
	ds_read_b128 v[232:235], v69 offset:57344
	ds_read_b128 v[236:239], v69 offset:61440
	ds_read_b128 v[240:243], v92 offset:57344
	ds_read_b128 v[244:247], v92 offset:61440
	s_waitcnt lgkmcnt(5)
	v_mfma_f32_32x32x16_bf16 v[2:17], v[62:65], v[2:5], 0
	v_mfma_f32_32x32x16_bf16 v[18:33], v[62:65], v[18:21], 0
	v_mfma_f32_32x32x16_bf16 v[2:17], v[58:61], v[100:103], v[2:17]
	s_waitcnt lgkmcnt(4)
	v_mfma_f32_32x32x16_bf16 v[18:33], v[58:61], v[228:231], v[18:33]
	s_waitcnt lgkmcnt(3)
	v_mfma_f32_32x32x16_bf16 v[2:17], v[54:57], v[232:235], v[2:17]
	s_waitcnt lgkmcnt(2)
	v_mfma_f32_32x32x16_bf16 v[18:33], v[54:57], v[236:239], v[18:33]
	s_waitcnt lgkmcnt(1)
	v_mfma_f32_32x32x16_bf16 v[2:17], v[50:53], v[240:243], v[2:17]
	s_waitcnt lgkmcnt(0)
	v_mfma_f32_32x32x16_bf16 v[18:33], v[50:53], v[244:247], v[18:33]
	s_nop 9
	v_max_i32_e32 v104, 0, v2
	v_max_i32_e32 v102, 0, v10
	v_max_i32_e32 v2, 0, v3
	v_max_i32_e32 v10, 0, v11
	v_max_i32_e32 v105, 0, v18
	v_pk_fma_f32 v[100:101], v[74:75], v[104:105], 0 op_sel_hi:[1,1,0]
	v_max_i32_e32 v103, 0, v26
	v_max_i32_e32 v3, 0, v19
	v_pk_fma_f32 v[102:103], v[76:77], v[102:103], 0 op_sel_hi:[1,1,0]
	v_pk_fma_f32 v[2:3], v[46:47], v[2:3], v[100:101]
	v_max_i32_e32 v11, 0, v27
	v_max_i32_e32 v18, 0, v4
	v_max_i32_e32 v19, 0, v20
	v_pk_fma_f32 v[10:11], v[42:43], v[10:11], v[102:103]
	v_pk_fma_f32 v[2:3], v[78:79], v[18:19], v[2:3]
	v_max_i32_e32 v18, 0, v12
	v_max_i32_e32 v19, 0, v28
	v_max_i32_e32 v4, 0, v5
	v_max_i32_e32 v5, 0, v21
	v_pk_fma_f32 v[10:11], v[80:81], v[18:19], v[10:11]
	v_pk_fma_f32 v[2:3], v[48:49], v[4:5], v[2:3]
	v_max_i32_e32 v4, 0, v13
	v_max_i32_e32 v5, 0, v29
	v_pk_fma_f32 v[4:5], v[44:45], v[4:5], v[10:11]
	v_max_i32_e32 v10, 0, v6
	v_max_i32_e32 v11, 0, v22
	v_pk_fma_f32 v[2:3], v[82:83], v[10:11], v[2:3]
	v_max_i32_e32 v10, 0, v14
	v_max_i32_e32 v11, 0, v30
	v_max_i32_e32 v6, 0, v7
	v_max_i32_e32 v7, 0, v23
	v_pk_fma_f32 v[4:5], v[84:85], v[10:11], v[4:5]
	v_pk_fma_f32 v[2:3], v[38:39], v[6:7], v[2:3]
	v_max_i32_e32 v6, 0, v15
	v_max_i32_e32 v7, 0, v31
	v_pk_fma_f32 v[4:5], v[34:35], v[6:7], v[4:5]
	v_max_i32_e32 v6, 0, v8
	v_max_i32_e32 v7, 0, v24
	v_pk_fma_f32 v[2:3], v[86:87], v[6:7], v[2:3]
	v_max_i32_e32 v6, 0, v16
	v_max_i32_e32 v7, 0, v32
	v_pk_fma_f32 v[4:5], v[88:89], v[6:7], v[4:5]
	v_max_i32_e32 v6, 0, v9
	v_max_i32_e32 v7, 0, v25
	v_pk_fma_f32 v[2:3], v[40:41], v[6:7], v[2:3]
	v_max_i32_e32 v6, 0, v17
	v_max_i32_e32 v7, 0, v33
	v_pk_fma_f32 v[4:5], v[36:37], v[6:7], v[4:5]
	v_not_b32_e32 v6, v2
	v_or_b32_e32 v7, 0x80000000, v2
	v_cmp_gt_i32_e32 vcc, 0, v2
	v_not_b32_e32 v2, v3
	s_nop 0
	v_cndmask_b32_e32 v190, v7, v6, vcc
	v_or_b32_e32 v6, 0x80000000, v3
	v_cmp_gt_i32_e32 vcc, 0, v3
	v_or_b32_e32 v3, 0x80000000, v4
	s_nop 0
	v_cndmask_b32_e32 v124, v6, v2, vcc
	v_not_b32_e32 v2, v4
	v_cmp_gt_i32_e32 vcc, 0, v4
	v_permlane32_swap_b32_e32 v190, v124
	s_nop 0
	v_cndmask_b32_e32 v153, v3, v2, vcc
	v_not_b32_e32 v2, v5
	v_or_b32_e32 v3, 0x80000000, v5
	v_cmp_gt_i32_e32 vcc, 0, v5
	s_nop 1
	v_cndmask_b32_e32 v100, v3, v2, vcc
	s_nop 1
	v_permlane32_swap_b32_e32 v153, v100

.LBB0_1110:
	ds_read_b128 v[2:5], v1
	ds_read_b128 v[18:21], v1 offset:4096
	ds_read_b128 v[102:105], v67
	ds_read_b128 v[228:231], v67 offset:4096
	ds_read_b128 v[232:235], v69
	ds_read_b128 v[236:239], v69 offset:4096
	ds_read_b128 v[240:243], v92
	ds_read_b128 v[244:247], v92 offset:4096
	s_waitcnt lgkmcnt(5)
	v_mfma_f32_32x32x16_bf16 v[2:17], v[62:65], v[2:5], 0
	v_mfma_f32_32x32x16_bf16 v[18:33], v[62:65], v[18:21], 0
	v_mfma_f32_32x32x16_bf16 v[2:17], v[58:61], v[102:105], v[2:17]
	s_waitcnt lgkmcnt(4)
	v_mfma_f32_32x32x16_bf16 v[18:33], v[58:61], v[228:231], v[18:33]
	s_waitcnt lgkmcnt(3)
	v_mfma_f32_32x32x16_bf16 v[2:17], v[54:57], v[232:235], v[2:17]
	s_waitcnt lgkmcnt(2)
	v_mfma_f32_32x32x16_bf16 v[18:33], v[54:57], v[236:239], v[18:33]
	s_waitcnt lgkmcnt(1)
	v_mfma_f32_32x32x16_bf16 v[2:17], v[50:53], v[240:243], v[2:17]
	s_waitcnt lgkmcnt(0)
	v_mfma_f32_32x32x16_bf16 v[18:33], v[50:53], v[244:247], v[18:33]
	s_nop 9
	v_max_i32_e32 v106, 0, v2
	v_max_i32_e32 v104, 0, v10
	v_max_i32_e32 v2, 0, v3
	v_max_i32_e32 v10, 0, v11
	v_max_i32_e32 v107, 0, v18
	v_pk_fma_f32 v[102:103], v[74:75], v[106:107], 0 op_sel_hi:[1,1,0]
	v_max_i32_e32 v105, 0, v26
	v_max_i32_e32 v3, 0, v19
	v_pk_fma_f32 v[104:105], v[76:77], v[104:105], 0 op_sel_hi:[1,1,0]
	v_pk_fma_f32 v[2:3], v[46:47], v[2:3], v[102:103]
	v_max_i32_e32 v11, 0, v27
	v_max_i32_e32 v18, 0, v4
	v_max_i32_e32 v19, 0, v20
	v_pk_fma_f32 v[10:11], v[42:43], v[10:11], v[104:105]
	v_pk_fma_f32 v[2:3], v[78:79], v[18:19], v[2:3]
	v_max_i32_e32 v18, 0, v12
	v_max_i32_e32 v19, 0, v28
	v_max_i32_e32 v4, 0, v5
	v_max_i32_e32 v5, 0, v21
	v_pk_fma_f32 v[10:11], v[80:81], v[18:19], v[10:11]
	v_pk_fma_f32 v[2:3], v[48:49], v[4:5], v[2:3]
	v_max_i32_e32 v4, 0, v13
	v_max_i32_e32 v5, 0, v29
	v_pk_fma_f32 v[4:5], v[44:45], v[4:5], v[10:11]
	v_max_i32_e32 v10, 0, v6
	v_max_i32_e32 v11, 0, v22
	v_pk_fma_f32 v[2:3], v[82:83], v[10:11], v[2:3]
	v_max_i32_e32 v10, 0, v14
	v_max_i32_e32 v11, 0, v30
	v_max_i32_e32 v6, 0, v7
	v_max_i32_e32 v7, 0, v23
	v_pk_fma_f32 v[4:5], v[84:85], v[10:11], v[4:5]
	v_pk_fma_f32 v[2:3], v[38:39], v[6:7], v[2:3]
	v_max_i32_e32 v6, 0, v15
	v_max_i32_e32 v7, 0, v31
	v_pk_fma_f32 v[4:5], v[34:35], v[6:7], v[4:5]
	v_max_i32_e32 v6, 0, v8
	v_max_i32_e32 v7, 0, v24
	v_pk_fma_f32 v[2:3], v[86:87], v[6:7], v[2:3]
	v_max_i32_e32 v6, 0, v16
	v_max_i32_e32 v7, 0, v32
	v_pk_fma_f32 v[4:5], v[88:89], v[6:7], v[4:5]
	v_max_i32_e32 v6, 0, v9
	v_max_i32_e32 v7, 0, v25
	v_pk_fma_f32 v[2:3], v[40:41], v[6:7], v[2:3]
	v_max_i32_e32 v6, 0, v17
	v_max_i32_e32 v7, 0, v33
	v_pk_fma_f32 v[4:5], v[36:37], v[6:7], v[4:5]
	v_not_b32_e32 v6, v2
	v_or_b32_e32 v7, 0x80000000, v2
	v_cmp_gt_i32_e32 vcc, 0, v2
	v_not_b32_e32 v2, v3
	s_nop 0
	v_cndmask_b32_e32 v191, v7, v6, vcc
	v_or_b32_e32 v6, 0x80000000, v3
	v_cmp_gt_i32_e32 vcc, 0, v3
	v_or_b32_e32 v3, 0x80000000, v4
	s_nop 0
	v_cndmask_b32_e32 v125, v6, v2, vcc
	v_not_b32_e32 v2, v4
	v_cmp_gt_i32_e32 vcc, 0, v4
	v_permlane32_swap_b32_e32 v191, v125
	s_nop 0
	v_cndmask_b32_e32 v154, v3, v2, vcc
	v_not_b32_e32 v2, v5
	v_or_b32_e32 v3, 0x80000000, v5
	v_cmp_gt_i32_e32 vcc, 0, v5
	s_nop 1
	v_cndmask_b32_e32 v101, v3, v2, vcc
	s_nop 1
	v_permlane32_swap_b32_e32 v154, v101

.LBB0_1136:
	ds_read_b128 v[2:5], v1 offset:8192
	ds_read_b128 v[18:21], v1 offset:12288
	ds_read_b128 v[102:105], v67 offset:8192
	ds_read_b128 v[228:231], v67 offset:12288
	ds_read_b128 v[232:235], v69 offset:8192
	ds_read_b128 v[236:239], v69 offset:12288
	ds_read_b128 v[240:243], v92 offset:8192
	ds_read_b128 v[244:247], v92 offset:12288
	s_waitcnt lgkmcnt(5)
	v_mfma_f32_32x32x16_bf16 v[2:17], v[62:65], v[2:5], 0
	v_mfma_f32_32x32x16_bf16 v[18:33], v[62:65], v[18:21], 0
	v_mfma_f32_32x32x16_bf16 v[2:17], v[58:61], v[102:105], v[2:17]
	s_waitcnt lgkmcnt(4)
	v_mfma_f32_32x32x16_bf16 v[18:33], v[58:61], v[228:231], v[18:33]
	s_waitcnt lgkmcnt(3)
	v_mfma_f32_32x32x16_bf16 v[2:17], v[54:57], v[232:235], v[2:17]
	s_waitcnt lgkmcnt(2)
	v_mfma_f32_32x32x16_bf16 v[18:33], v[54:57], v[236:239], v[18:33]
	s_waitcnt lgkmcnt(1)
	v_mfma_f32_32x32x16_bf16 v[2:17], v[50:53], v[240:243], v[2:17]
	s_waitcnt lgkmcnt(0)
	v_mfma_f32_32x32x16_bf16 v[18:33], v[50:53], v[244:247], v[18:33]
	s_nop 9
	v_max_i32_e32 v106, 0, v2
	v_max_i32_e32 v104, 0, v10
	v_max_i32_e32 v2, 0, v3
	v_max_i32_e32 v10, 0, v11
	v_max_i32_e32 v107, 0, v18
	v_pk_fma_f32 v[102:103], v[74:75], v[106:107], 0 op_sel_hi:[1,1,0]
	v_max_i32_e32 v105, 0, v26
	v_max_i32_e32 v3, 0, v19
	v_pk_fma_f32 v[104:105], v[76:77], v[104:105], 0 op_sel_hi:[1,1,0]
	v_pk_fma_f32 v[2:3], v[46:47], v[2:3], v[102:103]
	v_max_i32_e32 v11, 0, v27
	v_max_i32_e32 v18, 0, v4
	v_max_i32_e32 v19, 0, v20
	v_pk_fma_f32 v[10:11], v[42:43], v[10:11], v[104:105]
	v_pk_fma_f32 v[2:3], v[78:79], v[18:19], v[2:3]
	v_max_i32_e32 v18, 0, v12
	v_max_i32_e32 v19, 0, v28
	v_max_i32_e32 v4, 0, v5
	v_max_i32_e32 v5, 0, v21
	v_pk_fma_f32 v[10:11], v[80:81], v[18:19], v[10:11]
	v_pk_fma_f32 v[2:3], v[48:49], v[4:5], v[2:3]
	v_max_i32_e32 v4, 0, v13
	v_max_i32_e32 v5, 0, v29
	v_pk_fma_f32 v[4:5], v[44:45], v[4:5], v[10:11]
	v_max_i32_e32 v10, 0, v6
	v_max_i32_e32 v11, 0, v22
	v_pk_fma_f32 v[2:3], v[82:83], v[10:11], v[2:3]
	v_max_i32_e32 v10, 0, v14
	v_max_i32_e32 v11, 0, v30
	v_max_i32_e32 v6, 0, v7
	v_max_i32_e32 v7, 0, v23
	v_pk_fma_f32 v[4:5], v[84:85], v[10:11], v[4:5]
	v_pk_fma_f32 v[2:3], v[38:39], v[6:7], v[2:3]
	v_max_i32_e32 v6, 0, v15
	v_max_i32_e32 v7, 0, v31
	v_pk_fma_f32 v[4:5], v[34:35], v[6:7], v[4:5]
	v_max_i32_e32 v6, 0, v8
	v_max_i32_e32 v7, 0, v24
	v_pk_fma_f32 v[2:3], v[86:87], v[6:7], v[2:3]
	v_max_i32_e32 v6, 0, v16
	v_max_i32_e32 v7, 0, v32
	v_pk_fma_f32 v[4:5], v[88:89], v[6:7], v[4:5]
	v_max_i32_e32 v6, 0, v9
	v_max_i32_e32 v7, 0, v25
	v_pk_fma_f32 v[2:3], v[40:41], v[6:7], v[2:3]
	v_max_i32_e32 v6, 0, v17
	v_max_i32_e32 v7, 0, v33
	v_pk_fma_f32 v[4:5], v[36:37], v[6:7], v[4:5]
	v_not_b32_e32 v6, v2
	v_or_b32_e32 v7, 0x80000000, v2
	v_cmp_gt_i32_e32 vcc, 0, v2
	v_not_b32_e32 v2, v3
	s_nop 0
	v_cndmask_b32_e32 v192, v7, v6, vcc
	v_or_b32_e32 v6, 0x80000000, v3
	v_cmp_gt_i32_e32 vcc, 0, v3
	v_or_b32_e32 v3, 0x80000000, v4
	s_nop 0
	v_cndmask_b32_e32 v126, v6, v2, vcc
	v_not_b32_e32 v2, v4
	v_cmp_gt_i32_e32 vcc, 0, v4
	v_permlane32_swap_b32_e32 v192, v126
	s_nop 0
	v_cndmask_b32_e32 v155, v3, v2, vcc
	v_not_b32_e32 v2, v5
	v_or_b32_e32 v3, 0x80000000, v5
	v_cmp_gt_i32_e32 vcc, 0, v5
	s_nop 1
	v_cndmask_b32_e32 v102, v3, v2, vcc
	s_nop 1
	v_permlane32_swap_b32_e32 v155, v102

.LBB0_1162:
	ds_read_b128 v[2:5], v1 offset:16384
	ds_read_b128 v[18:21], v1 offset:20480
	ds_read_b128 v[104:107], v67 offset:16384
	ds_read_b128 v[228:231], v67 offset:20480
	ds_read_b128 v[232:235], v69 offset:16384
	ds_read_b128 v[236:239], v69 offset:20480
	ds_read_b128 v[240:243], v92 offset:16384
	ds_read_b128 v[244:247], v92 offset:20480
	s_waitcnt lgkmcnt(5)
	v_mfma_f32_32x32x16_bf16 v[2:17], v[62:65], v[2:5], 0
	v_mfma_f32_32x32x16_bf16 v[18:33], v[62:65], v[18:21], 0
	v_mfma_f32_32x32x16_bf16 v[2:17], v[58:61], v[104:107], v[2:17]
	s_waitcnt lgkmcnt(4)
	v_mfma_f32_32x32x16_bf16 v[18:33], v[58:61], v[228:231], v[18:33]
	s_waitcnt lgkmcnt(3)
	v_mfma_f32_32x32x16_bf16 v[2:17], v[54:57], v[232:235], v[2:17]
	s_waitcnt lgkmcnt(2)
	v_mfma_f32_32x32x16_bf16 v[18:33], v[54:57], v[236:239], v[18:33]
	s_waitcnt lgkmcnt(1)
	v_mfma_f32_32x32x16_bf16 v[2:17], v[50:53], v[240:243], v[2:17]
	s_waitcnt lgkmcnt(0)
	v_mfma_f32_32x32x16_bf16 v[18:33], v[50:53], v[244:247], v[18:33]
	s_nop 9
	v_max_i32_e32 v108, 0, v2
	v_max_i32_e32 v106, 0, v10
	v_max_i32_e32 v2, 0, v3
	v_max_i32_e32 v10, 0, v11
	v_max_i32_e32 v109, 0, v18
	v_pk_fma_f32 v[104:105], v[74:75], v[108:109], 0 op_sel_hi:[1,1,0]
	v_max_i32_e32 v107, 0, v26
	v_max_i32_e32 v3, 0, v19
	v_pk_fma_f32 v[106:107], v[76:77], v[106:107], 0 op_sel_hi:[1,1,0]
	v_pk_fma_f32 v[2:3], v[46:47], v[2:3], v[104:105]
	v_max_i32_e32 v11, 0, v27
	v_max_i32_e32 v18, 0, v4
	v_max_i32_e32 v19, 0, v20
	v_pk_fma_f32 v[10:11], v[42:43], v[10:11], v[106:107]
	v_pk_fma_f32 v[2:3], v[78:79], v[18:19], v[2:3]
	v_max_i32_e32 v18, 0, v12
	v_max_i32_e32 v19, 0, v28
	v_max_i32_e32 v4, 0, v5
	v_max_i32_e32 v5, 0, v21
	v_pk_fma_f32 v[10:11], v[80:81], v[18:19], v[10:11]
	v_pk_fma_f32 v[2:3], v[48:49], v[4:5], v[2:3]
	v_max_i32_e32 v4, 0, v13
	v_max_i32_e32 v5, 0, v29
	v_pk_fma_f32 v[4:5], v[44:45], v[4:5], v[10:11]
	v_max_i32_e32 v10, 0, v6
	v_max_i32_e32 v11, 0, v22
	v_pk_fma_f32 v[2:3], v[82:83], v[10:11], v[2:3]
	v_max_i32_e32 v10, 0, v14
	v_max_i32_e32 v11, 0, v30
	v_max_i32_e32 v6, 0, v7
	v_max_i32_e32 v7, 0, v23
	v_pk_fma_f32 v[4:5], v[84:85], v[10:11], v[4:5]
	v_pk_fma_f32 v[2:3], v[38:39], v[6:7], v[2:3]
	v_max_i32_e32 v6, 0, v15
	v_max_i32_e32 v7, 0, v31
	v_pk_fma_f32 v[4:5], v[34:35], v[6:7], v[4:5]
	v_max_i32_e32 v6, 0, v8
	v_max_i32_e32 v7, 0, v24
	v_pk_fma_f32 v[2:3], v[86:87], v[6:7], v[2:3]
	v_max_i32_e32 v6, 0, v16
	v_max_i32_e32 v7, 0, v32
	v_pk_fma_f32 v[4:5], v[88:89], v[6:7], v[4:5]
	v_max_i32_e32 v6, 0, v9
	v_max_i32_e32 v7, 0, v25
	v_pk_fma_f32 v[2:3], v[40:41], v[6:7], v[2:3]
	v_max_i32_e32 v6, 0, v17
	v_max_i32_e32 v7, 0, v33
	v_pk_fma_f32 v[4:5], v[36:37], v[6:7], v[4:5]
	v_not_b32_e32 v6, v2
	v_or_b32_e32 v7, 0x80000000, v2
	v_cmp_gt_i32_e32 vcc, 0, v2
	v_not_b32_e32 v2, v3
	s_nop 0
	v_cndmask_b32_e32 v193, v7, v6, vcc
	v_or_b32_e32 v6, 0x80000000, v3
	v_cmp_gt_i32_e32 vcc, 0, v3
	v_or_b32_e32 v3, 0x80000000, v4
	s_nop 0
	v_cndmask_b32_e32 v127, v6, v2, vcc
	v_not_b32_e32 v2, v4
	v_cmp_gt_i32_e32 vcc, 0, v4
	v_permlane32_swap_b32_e32 v193, v127
	s_nop 0
	v_cndmask_b32_e32 v156, v3, v2, vcc
	v_not_b32_e32 v2, v5
	v_or_b32_e32 v3, 0x80000000, v5
	v_cmp_gt_i32_e32 vcc, 0, v5
	s_nop 1
	v_cndmask_b32_e32 v103, v3, v2, vcc
	s_nop 1
	v_permlane32_swap_b32_e32 v156, v103

.LBB0_1188:
	ds_read_b128 v[2:5], v1 offset:24576
	ds_read_b128 v[18:21], v1 offset:28672
	ds_read_b128 v[104:107], v67 offset:24576
	ds_read_b128 v[228:231], v67 offset:28672
	ds_read_b128 v[232:235], v69 offset:24576
	ds_read_b128 v[236:239], v69 offset:28672
	ds_read_b128 v[240:243], v92 offset:24576
	ds_read_b128 v[244:247], v92 offset:28672
	s_waitcnt lgkmcnt(5)
	v_mfma_f32_32x32x16_bf16 v[2:17], v[62:65], v[2:5], 0
	v_mfma_f32_32x32x16_bf16 v[18:33], v[62:65], v[18:21], 0
	v_mfma_f32_32x32x16_bf16 v[2:17], v[58:61], v[104:107], v[2:17]
	s_waitcnt lgkmcnt(4)
	v_mfma_f32_32x32x16_bf16 v[18:33], v[58:61], v[228:231], v[18:33]
	s_waitcnt lgkmcnt(3)
	v_mfma_f32_32x32x16_bf16 v[2:17], v[54:57], v[232:235], v[2:17]
	s_waitcnt lgkmcnt(2)
	v_mfma_f32_32x32x16_bf16 v[18:33], v[54:57], v[236:239], v[18:33]
	s_waitcnt lgkmcnt(1)
	v_mfma_f32_32x32x16_bf16 v[2:17], v[50:53], v[240:243], v[2:17]
	s_waitcnt lgkmcnt(0)
	v_mfma_f32_32x32x16_bf16 v[18:33], v[50:53], v[244:247], v[18:33]
	s_nop 9
	v_max_i32_e32 v108, 0, v2
	v_max_i32_e32 v106, 0, v10
	v_max_i32_e32 v2, 0, v3
	v_max_i32_e32 v10, 0, v11
	v_max_i32_e32 v109, 0, v18
	v_pk_fma_f32 v[104:105], v[74:75], v[108:109], 0 op_sel_hi:[1,1,0]
	v_max_i32_e32 v107, 0, v26
	v_max_i32_e32 v3, 0, v19
	v_pk_fma_f32 v[106:107], v[76:77], v[106:107], 0 op_sel_hi:[1,1,0]
	v_pk_fma_f32 v[2:3], v[46:47], v[2:3], v[104:105]
	v_max_i32_e32 v11, 0, v27
	v_max_i32_e32 v18, 0, v4
	v_max_i32_e32 v19, 0, v20
	v_pk_fma_f32 v[10:11], v[42:43], v[10:11], v[106:107]
	v_pk_fma_f32 v[2:3], v[78:79], v[18:19], v[2:3]
	v_max_i32_e32 v18, 0, v12
	v_max_i32_e32 v19, 0, v28
	v_max_i32_e32 v4, 0, v5
	v_max_i32_e32 v5, 0, v21
	v_pk_fma_f32 v[10:11], v[80:81], v[18:19], v[10:11]
	v_pk_fma_f32 v[2:3], v[48:49], v[4:5], v[2:3]
	v_max_i32_e32 v4, 0, v13
	v_max_i32_e32 v5, 0, v29
	v_pk_fma_f32 v[4:5], v[44:45], v[4:5], v[10:11]
	v_max_i32_e32 v10, 0, v6
	v_max_i32_e32 v11, 0, v22
	v_pk_fma_f32 v[2:3], v[82:83], v[10:11], v[2:3]
	v_max_i32_e32 v10, 0, v14
	v_max_i32_e32 v11, 0, v30
	v_max_i32_e32 v6, 0, v7
	v_max_i32_e32 v7, 0, v23
	v_pk_fma_f32 v[4:5], v[84:85], v[10:11], v[4:5]
	v_pk_fma_f32 v[2:3], v[38:39], v[6:7], v[2:3]
	v_max_i32_e32 v6, 0, v15
	v_max_i32_e32 v7, 0, v31
	v_pk_fma_f32 v[4:5], v[34:35], v[6:7], v[4:5]
	v_max_i32_e32 v6, 0, v8
	v_max_i32_e32 v7, 0, v24
	v_pk_fma_f32 v[2:3], v[86:87], v[6:7], v[2:3]
	v_max_i32_e32 v6, 0, v16
	v_max_i32_e32 v7, 0, v32
	v_pk_fma_f32 v[4:5], v[88:89], v[6:7], v[4:5]
	v_max_i32_e32 v6, 0, v9
	v_max_i32_e32 v7, 0, v25
	v_pk_fma_f32 v[2:3], v[40:41], v[6:7], v[2:3]
	v_max_i32_e32 v6, 0, v17
	v_max_i32_e32 v7, 0, v33
	v_pk_fma_f32 v[4:5], v[36:37], v[6:7], v[4:5]
	v_not_b32_e32 v6, v2
	v_or_b32_e32 v7, 0x80000000, v2
	v_cmp_gt_i32_e32 vcc, 0, v2
	v_not_b32_e32 v2, v3
	s_nop 0
	v_cndmask_b32_e32 v194, v7, v6, vcc
	v_or_b32_e32 v6, 0x80000000, v3
	v_cmp_gt_i32_e32 vcc, 0, v3
	v_or_b32_e32 v3, 0x80000000, v4
	s_nop 0
	v_cndmask_b32_e32 v128, v6, v2, vcc
	v_not_b32_e32 v2, v4
	v_cmp_gt_i32_e32 vcc, 0, v4
	v_permlane32_swap_b32_e32 v194, v128
	s_nop 0
	v_cndmask_b32_e32 v157, v3, v2, vcc
	v_not_b32_e32 v2, v5
	v_or_b32_e32 v3, 0x80000000, v5
	v_cmp_gt_i32_e32 vcc, 0, v5
	s_nop 1
	v_cndmask_b32_e32 v104, v3, v2, vcc
	s_nop 1
	v_permlane32_swap_b32_e32 v157, v104

.LBB0_1214:
	ds_read_b128 v[2:5], v1 offset:32768
	ds_read_b128 v[18:21], v1 offset:36864
	ds_read_b128 v[106:109], v67 offset:32768
	ds_read_b128 v[228:231], v67 offset:36864
	ds_read_b128 v[232:235], v69 offset:32768
	ds_read_b128 v[236:239], v69 offset:36864
	ds_read_b128 v[240:243], v92 offset:32768
	ds_read_b128 v[244:247], v92 offset:36864
	s_waitcnt lgkmcnt(5)
	v_mfma_f32_32x32x16_bf16 v[2:17], v[62:65], v[2:5], 0
	v_mfma_f32_32x32x16_bf16 v[18:33], v[62:65], v[18:21], 0
	v_mfma_f32_32x32x16_bf16 v[2:17], v[58:61], v[106:109], v[2:17]
	s_waitcnt lgkmcnt(4)
	v_mfma_f32_32x32x16_bf16 v[18:33], v[58:61], v[228:231], v[18:33]
	s_waitcnt lgkmcnt(3)
	v_mfma_f32_32x32x16_bf16 v[2:17], v[54:57], v[232:235], v[2:17]
	s_waitcnt lgkmcnt(2)
	v_mfma_f32_32x32x16_bf16 v[18:33], v[54:57], v[236:239], v[18:33]
	s_waitcnt lgkmcnt(1)
	v_mfma_f32_32x32x16_bf16 v[2:17], v[50:53], v[240:243], v[2:17]
	s_waitcnt lgkmcnt(0)
	v_mfma_f32_32x32x16_bf16 v[18:33], v[50:53], v[244:247], v[18:33]
	s_nop 9
	v_max_i32_e32 v130, 0, v2
	v_max_i32_e32 v108, 0, v10
	v_max_i32_e32 v2, 0, v3
	v_max_i32_e32 v10, 0, v11
	v_max_i32_e32 v131, 0, v18
	v_pk_fma_f32 v[106:107], v[74:75], v[130:131], 0 op_sel_hi:[1,1,0]
	v_max_i32_e32 v109, 0, v26
	v_max_i32_e32 v3, 0, v19
	v_pk_fma_f32 v[108:109], v[76:77], v[108:109], 0 op_sel_hi:[1,1,0]
	v_pk_fma_f32 v[2:3], v[46:47], v[2:3], v[106:107]
	v_max_i32_e32 v11, 0, v27
	v_max_i32_e32 v18, 0, v4
	v_max_i32_e32 v19, 0, v20
	v_pk_fma_f32 v[10:11], v[42:43], v[10:11], v[108:109]
	v_pk_fma_f32 v[2:3], v[78:79], v[18:19], v[2:3]
	v_max_i32_e32 v18, 0, v12
	v_max_i32_e32 v19, 0, v28
	v_max_i32_e32 v4, 0, v5
	v_max_i32_e32 v5, 0, v21
	v_pk_fma_f32 v[10:11], v[80:81], v[18:19], v[10:11]
	v_pk_fma_f32 v[2:3], v[48:49], v[4:5], v[2:3]
	v_max_i32_e32 v4, 0, v13
	v_max_i32_e32 v5, 0, v29
	v_pk_fma_f32 v[4:5], v[44:45], v[4:5], v[10:11]
	v_max_i32_e32 v10, 0, v6
	v_max_i32_e32 v11, 0, v22
	v_pk_fma_f32 v[2:3], v[82:83], v[10:11], v[2:3]
	v_max_i32_e32 v10, 0, v14
	v_max_i32_e32 v11, 0, v30
	v_max_i32_e32 v6, 0, v7
	v_max_i32_e32 v7, 0, v23
	v_pk_fma_f32 v[4:5], v[84:85], v[10:11], v[4:5]
	v_pk_fma_f32 v[2:3], v[38:39], v[6:7], v[2:3]
	v_max_i32_e32 v6, 0, v15
	v_max_i32_e32 v7, 0, v31
	v_pk_fma_f32 v[4:5], v[34:35], v[6:7], v[4:5]
	v_max_i32_e32 v6, 0, v8
	v_max_i32_e32 v7, 0, v24
	v_pk_fma_f32 v[2:3], v[86:87], v[6:7], v[2:3]
	v_max_i32_e32 v6, 0, v16
	v_max_i32_e32 v7, 0, v32
	v_pk_fma_f32 v[4:5], v[88:89], v[6:7], v[4:5]
	v_max_i32_e32 v6, 0, v9
	v_max_i32_e32 v7, 0, v25
	v_pk_fma_f32 v[2:3], v[40:41], v[6:7], v[2:3]
	v_max_i32_e32 v6, 0, v17
	v_max_i32_e32 v7, 0, v33
	v_pk_fma_f32 v[4:5], v[36:37], v[6:7], v[4:5]
	v_not_b32_e32 v6, v2
	v_or_b32_e32 v7, 0x80000000, v2
	v_cmp_gt_i32_e32 vcc, 0, v2
	v_not_b32_e32 v2, v3
	s_nop 0
	v_cndmask_b32_e32 v195, v7, v6, vcc
	v_or_b32_e32 v6, 0x80000000, v3
	v_cmp_gt_i32_e32 vcc, 0, v3
	v_or_b32_e32 v3, 0x80000000, v4
	s_nop 0
	v_cndmask_b32_e32 v129, v6, v2, vcc
	v_not_b32_e32 v2, v4
	v_cmp_gt_i32_e32 vcc, 0, v4
	v_permlane32_swap_b32_e32 v195, v129
	s_nop 0
	v_cndmask_b32_e32 v158, v3, v2, vcc
	v_not_b32_e32 v2, v5
	v_or_b32_e32 v3, 0x80000000, v5
	v_cmp_gt_i32_e32 vcc, 0, v5
	s_nop 1
	v_cndmask_b32_e32 v105, v3, v2, vcc
	s_nop 1
	v_permlane32_swap_b32_e32 v158, v105

.LBB0_1240:
	ds_read_b128 v[2:5], v1 offset:40960
	ds_read_b128 v[18:21], v1 offset:45056
	ds_read_b128 v[106:109], v67 offset:40960
	ds_read_b128 v[228:231], v67 offset:45056
	ds_read_b128 v[232:235], v69 offset:40960
	ds_read_b128 v[236:239], v69 offset:45056
	ds_read_b128 v[240:243], v92 offset:40960
	ds_read_b128 v[244:247], v92 offset:45056
	s_waitcnt lgkmcnt(5)
	v_mfma_f32_32x32x16_bf16 v[2:17], v[62:65], v[2:5], 0
	v_mfma_f32_32x32x16_bf16 v[18:33], v[62:65], v[18:21], 0
	v_mfma_f32_32x32x16_bf16 v[2:17], v[58:61], v[106:109], v[2:17]
	s_waitcnt lgkmcnt(4)
	v_mfma_f32_32x32x16_bf16 v[18:33], v[58:61], v[228:231], v[18:33]
	s_waitcnt lgkmcnt(3)
	v_mfma_f32_32x32x16_bf16 v[2:17], v[54:57], v[232:235], v[2:17]
	s_waitcnt lgkmcnt(2)
	v_mfma_f32_32x32x16_bf16 v[18:33], v[54:57], v[236:239], v[18:33]
	s_waitcnt lgkmcnt(1)
	v_mfma_f32_32x32x16_bf16 v[2:17], v[50:53], v[240:243], v[2:17]
	s_waitcnt lgkmcnt(0)
	v_mfma_f32_32x32x16_bf16 v[18:33], v[50:53], v[244:247], v[18:33]
	s_nop 9
	v_max_i32_e32 v130, 0, v2
	v_max_i32_e32 v108, 0, v10
	v_max_i32_e32 v2, 0, v3
	v_max_i32_e32 v10, 0, v11
	v_max_i32_e32 v131, 0, v18
	v_pk_fma_f32 v[106:107], v[74:75], v[130:131], 0 op_sel_hi:[1,1,0]
	v_max_i32_e32 v109, 0, v26
	v_max_i32_e32 v3, 0, v19
	v_pk_fma_f32 v[108:109], v[76:77], v[108:109], 0 op_sel_hi:[1,1,0]
	v_pk_fma_f32 v[2:3], v[46:47], v[2:3], v[106:107]
	v_max_i32_e32 v11, 0, v27
	v_max_i32_e32 v18, 0, v4
	v_max_i32_e32 v19, 0, v20
	v_pk_fma_f32 v[10:11], v[42:43], v[10:11], v[108:109]
	v_pk_fma_f32 v[2:3], v[78:79], v[18:19], v[2:3]
	v_max_i32_e32 v18, 0, v12
	v_max_i32_e32 v19, 0, v28
	v_max_i32_e32 v4, 0, v5
	v_max_i32_e32 v5, 0, v21
	v_pk_fma_f32 v[10:11], v[80:81], v[18:19], v[10:11]
	v_pk_fma_f32 v[2:3], v[48:49], v[4:5], v[2:3]
	v_max_i32_e32 v4, 0, v13
	v_max_i32_e32 v5, 0, v29
	v_pk_fma_f32 v[4:5], v[44:45], v[4:5], v[10:11]
	v_max_i32_e32 v10, 0, v6
	v_max_i32_e32 v11, 0, v22
	v_pk_fma_f32 v[2:3], v[82:83], v[10:11], v[2:3]
	v_max_i32_e32 v10, 0, v14
	v_max_i32_e32 v11, 0, v30
	v_max_i32_e32 v6, 0, v7
	v_max_i32_e32 v7, 0, v23
	v_pk_fma_f32 v[4:5], v[84:85], v[10:11], v[4:5]
	v_pk_fma_f32 v[2:3], v[38:39], v[6:7], v[2:3]
	v_max_i32_e32 v6, 0, v15
	v_max_i32_e32 v7, 0, v31
	v_pk_fma_f32 v[4:5], v[34:35], v[6:7], v[4:5]
	v_max_i32_e32 v6, 0, v8
	v_max_i32_e32 v7, 0, v24
	v_pk_fma_f32 v[2:3], v[86:87], v[6:7], v[2:3]
	v_max_i32_e32 v6, 0, v16
	v_max_i32_e32 v7, 0, v32
	v_pk_fma_f32 v[4:5], v[88:89], v[6:7], v[4:5]
	v_max_i32_e32 v6, 0, v9
	v_max_i32_e32 v7, 0, v25
	v_pk_fma_f32 v[2:3], v[40:41], v[6:7], v[2:3]
	v_max_i32_e32 v6, 0, v17
	v_max_i32_e32 v7, 0, v33
	v_pk_fma_f32 v[4:5], v[36:37], v[6:7], v[4:5]
	v_not_b32_e32 v6, v2
	v_or_b32_e32 v7, 0x80000000, v2
	v_cmp_gt_i32_e32 vcc, 0, v2
	v_not_b32_e32 v2, v3
	s_nop 0
	v_cndmask_b32_e32 v196, v7, v6, vcc
	v_or_b32_e32 v6, 0x80000000, v3
	v_cmp_gt_i32_e32 vcc, 0, v3
	v_or_b32_e32 v3, 0x80000000, v4
	s_nop 0
	v_cndmask_b32_e32 v130, v6, v2, vcc
	v_not_b32_e32 v2, v4
	v_cmp_gt_i32_e32 vcc, 0, v4
	v_permlane32_swap_b32_e32 v196, v130
	s_nop 0
	v_cndmask_b32_e32 v159, v3, v2, vcc
	v_not_b32_e32 v2, v5
	v_or_b32_e32 v3, 0x80000000, v5
	v_cmp_gt_i32_e32 vcc, 0, v5
	s_nop 1
	v_cndmask_b32_e32 v106, v3, v2, vcc
	s_nop 1
	v_permlane32_swap_b32_e32 v159, v106

.LBB0_1266:
	ds_read_b128 v[2:5], v1 offset:49152
	ds_read_b128 v[18:21], v1 offset:53248
	ds_read_b128 v[132:135], v67 offset:49152
	ds_read_b128 v[228:231], v67 offset:53248
	ds_read_b128 v[232:235], v69 offset:49152
	ds_read_b128 v[236:239], v69 offset:53248
	ds_read_b128 v[240:243], v92 offset:49152
	ds_read_b128 v[244:247], v92 offset:53248
	s_waitcnt lgkmcnt(5)
	v_mfma_f32_32x32x16_bf16 v[2:17], v[62:65], v[2:5], 0
	v_mfma_f32_32x32x16_bf16 v[18:33], v[62:65], v[18:21], 0
	v_mfma_f32_32x32x16_bf16 v[2:17], v[58:61], v[132:135], v[2:17]
	s_waitcnt lgkmcnt(4)
	v_mfma_f32_32x32x16_bf16 v[18:33], v[58:61], v[228:231], v[18:33]
	s_waitcnt lgkmcnt(3)
	v_mfma_f32_32x32x16_bf16 v[2:17], v[54:57], v[232:235], v[2:17]
	s_waitcnt lgkmcnt(2)
	v_mfma_f32_32x32x16_bf16 v[18:33], v[54:57], v[236:239], v[18:33]
	s_waitcnt lgkmcnt(1)
	v_mfma_f32_32x32x16_bf16 v[2:17], v[50:53], v[240:243], v[2:17]
	s_waitcnt lgkmcnt(0)
	v_mfma_f32_32x32x16_bf16 v[18:33], v[50:53], v[244:247], v[18:33]
	s_nop 9
	v_max_i32_e32 v108, 0, v2
	v_max_i32_e32 v132, 0, v10
	v_max_i32_e32 v2, 0, v3
	v_max_i32_e32 v10, 0, v11
	v_max_i32_e32 v109, 0, v18
	v_pk_fma_f32 v[108:109], v[74:75], v[108:109], 0 op_sel_hi:[1,1,0]
	v_max_i32_e32 v133, 0, v26
	v_max_i32_e32 v3, 0, v19
	v_pk_fma_f32 v[132:133], v[76:77], v[132:133], 0 op_sel_hi:[1,1,0]
	v_pk_fma_f32 v[2:3], v[46:47], v[2:3], v[108:109]
	v_max_i32_e32 v11, 0, v27
	v_max_i32_e32 v18, 0, v4
	v_max_i32_e32 v19, 0, v20
	v_pk_fma_f32 v[10:11], v[42:43], v[10:11], v[132:133]
	v_pk_fma_f32 v[2:3], v[78:79], v[18:19], v[2:3]
	v_max_i32_e32 v18, 0, v12
	v_max_i32_e32 v19, 0, v28
	v_max_i32_e32 v4, 0, v5
	v_max_i32_e32 v5, 0, v21
	v_pk_fma_f32 v[10:11], v[80:81], v[18:19], v[10:11]
	v_pk_fma_f32 v[2:3], v[48:49], v[4:5], v[2:3]
	v_max_i32_e32 v4, 0, v13
	v_max_i32_e32 v5, 0, v29
	v_pk_fma_f32 v[4:5], v[44:45], v[4:5], v[10:11]
	v_max_i32_e32 v10, 0, v6
	v_max_i32_e32 v11, 0, v22
	v_pk_fma_f32 v[2:3], v[82:83], v[10:11], v[2:3]
	v_max_i32_e32 v10, 0, v14
	v_max_i32_e32 v11, 0, v30
	v_max_i32_e32 v6, 0, v7
	v_max_i32_e32 v7, 0, v23
	v_pk_fma_f32 v[4:5], v[84:85], v[10:11], v[4:5]
	v_pk_fma_f32 v[2:3], v[38:39], v[6:7], v[2:3]
	v_max_i32_e32 v6, 0, v15
	v_max_i32_e32 v7, 0, v31
	v_pk_fma_f32 v[4:5], v[34:35], v[6:7], v[4:5]
	v_max_i32_e32 v6, 0, v8
	v_max_i32_e32 v7, 0, v24
	v_pk_fma_f32 v[2:3], v[86:87], v[6:7], v[2:3]
	v_max_i32_e32 v6, 0, v16
	v_max_i32_e32 v7, 0, v32
	v_pk_fma_f32 v[4:5], v[88:89], v[6:7], v[4:5]
	v_max_i32_e32 v6, 0, v9
	v_max_i32_e32 v7, 0, v25
	v_pk_fma_f32 v[2:3], v[40:41], v[6:7], v[2:3]
	v_max_i32_e32 v6, 0, v17
	v_max_i32_e32 v7, 0, v33
	v_pk_fma_f32 v[4:5], v[36:37], v[6:7], v[4:5]
	v_not_b32_e32 v6, v2
	v_or_b32_e32 v7, 0x80000000, v2
	v_cmp_gt_i32_e32 vcc, 0, v2
	v_not_b32_e32 v2, v3
	s_nop 0
	v_cndmask_b32_e32 v198, v7, v6, vcc
	v_or_b32_e32 v6, 0x80000000, v3
	v_cmp_gt_i32_e32 vcc, 0, v3
	v_or_b32_e32 v3, 0x80000000, v4
	s_nop 0
	v_cndmask_b32_e32 v132, v6, v2, vcc
	v_not_b32_e32 v2, v4
	v_cmp_gt_i32_e32 vcc, 0, v4
	v_permlane32_swap_b32_e32 v198, v132
	s_nop 0
	v_cndmask_b32_e32 v161, v3, v2, vcc
	v_not_b32_e32 v2, v5
	v_or_b32_e32 v3, 0x80000000, v5
	v_cmp_gt_i32_e32 vcc, 0, v5
	s_nop 1
	v_cndmask_b32_e32 v107, v3, v2, vcc
	s_nop 1
	v_permlane32_swap_b32_e32 v161, v107

.LBB0_1292:
	ds_read_b128 v[2:5], v1 offset:57344
	ds_read_b128 v[18:21], v1 offset:61440
	ds_read_b128 v[134:137], v67 offset:57344
	ds_read_b128 v[228:231], v67 offset:61440
	ds_read_b128 v[232:235], v69 offset:57344
	ds_read_b128 v[236:239], v69 offset:61440
	ds_read_b128 v[240:243], v92 offset:57344
	ds_read_b128 v[244:247], v92 offset:61440
	s_waitcnt lgkmcnt(5)
	v_mfma_f32_32x32x16_bf16 v[2:17], v[62:65], v[2:5], 0
	v_mfma_f32_32x32x16_bf16 v[18:33], v[62:65], v[18:21], 0
	v_mfma_f32_32x32x16_bf16 v[2:17], v[58:61], v[134:137], v[2:17]
	s_waitcnt lgkmcnt(4)
	v_mfma_f32_32x32x16_bf16 v[18:33], v[58:61], v[228:231], v[18:33]
	s_waitcnt lgkmcnt(3)
	v_mfma_f32_32x32x16_bf16 v[2:17], v[54:57], v[232:235], v[2:17]
	s_waitcnt lgkmcnt(2)
	v_mfma_f32_32x32x16_bf16 v[18:33], v[54:57], v[236:239], v[18:33]
	s_waitcnt lgkmcnt(1)
	v_mfma_f32_32x32x16_bf16 v[2:17], v[50:53], v[240:243], v[2:17]
	s_waitcnt lgkmcnt(0)
	v_mfma_f32_32x32x16_bf16 v[18:33], v[50:53], v[244:247], v[18:33]
	s_nop 9
	v_max_i32_e32 v108, 0, v2
	v_max_i32_e32 v134, 0, v10
	v_max_i32_e32 v2, 0, v3
	v_max_i32_e32 v10, 0, v11
	v_max_i32_e32 v109, 0, v18
	v_pk_fma_f32 v[108:109], v[74:75], v[108:109], 0 op_sel_hi:[1,1,0]
	v_max_i32_e32 v135, 0, v26
	v_max_i32_e32 v3, 0, v19
	v_pk_fma_f32 v[134:135], v[76:77], v[134:135], 0 op_sel_hi:[1,1,0]
	v_pk_fma_f32 v[2:3], v[46:47], v[2:3], v[108:109]
	v_max_i32_e32 v11, 0, v27
	v_max_i32_e32 v18, 0, v4
	v_max_i32_e32 v19, 0, v20
	v_pk_fma_f32 v[10:11], v[42:43], v[10:11], v[134:135]
	v_pk_fma_f32 v[2:3], v[78:79], v[18:19], v[2:3]
	v_max_i32_e32 v18, 0, v12
	v_max_i32_e32 v19, 0, v28
	v_max_i32_e32 v4, 0, v5
	v_max_i32_e32 v5, 0, v21
	v_pk_fma_f32 v[10:11], v[80:81], v[18:19], v[10:11]
	v_pk_fma_f32 v[2:3], v[48:49], v[4:5], v[2:3]
	v_max_i32_e32 v4, 0, v13
	v_max_i32_e32 v5, 0, v29
	v_pk_fma_f32 v[4:5], v[44:45], v[4:5], v[10:11]
	v_max_i32_e32 v10, 0, v6
	v_max_i32_e32 v11, 0, v22
	v_pk_fma_f32 v[2:3], v[82:83], v[10:11], v[2:3]
	v_max_i32_e32 v10, 0, v14
	v_max_i32_e32 v11, 0, v30
	v_max_i32_e32 v6, 0, v7
	v_max_i32_e32 v7, 0, v23
	v_pk_fma_f32 v[4:5], v[84:85], v[10:11], v[4:5]
	v_pk_fma_f32 v[2:3], v[38:39], v[6:7], v[2:3]
	v_max_i32_e32 v6, 0, v15
	v_max_i32_e32 v7, 0, v31
	v_pk_fma_f32 v[4:5], v[34:35], v[6:7], v[4:5]
	v_max_i32_e32 v6, 0, v8
	v_max_i32_e32 v7, 0, v24
	v_pk_fma_f32 v[2:3], v[86:87], v[6:7], v[2:3]
	v_max_i32_e32 v6, 0, v16
	v_max_i32_e32 v7, 0, v32
	v_pk_fma_f32 v[4:5], v[88:89], v[6:7], v[4:5]
	v_max_i32_e32 v6, 0, v9
	v_max_i32_e32 v7, 0, v25
	v_pk_fma_f32 v[2:3], v[40:41], v[6:7], v[2:3]
	v_max_i32_e32 v6, 0, v17
	v_max_i32_e32 v7, 0, v33
	v_pk_fma_f32 v[4:5], v[36:37], v[6:7], v[4:5]
	v_not_b32_e32 v6, v2
	v_or_b32_e32 v7, 0x80000000, v2
	v_cmp_gt_i32_e32 vcc, 0, v2
	v_not_b32_e32 v2, v3
	s_nop 0
	v_cndmask_b32_e32 v200, v7, v6, vcc
	v_or_b32_e32 v6, 0x80000000, v3
	v_cmp_gt_i32_e32 vcc, 0, v3
	v_or_b32_e32 v3, 0x80000000, v4
	s_nop 0
	v_cndmask_b32_e32 v133, v6, v2, vcc
	v_not_b32_e32 v2, v4
	v_cmp_gt_i32_e32 vcc, 0, v4
	v_permlane32_swap_b32_e32 v200, v133
	s_nop 0
	v_cndmask_b32_e32 v164, v3, v2, vcc
	v_not_b32_e32 v2, v5
	v_or_b32_e32 v3, 0x80000000, v5
	v_cmp_gt_i32_e32 vcc, 0, v5
	s_nop 1
	v_cndmask_b32_e32 v108, v3, v2, vcc
	s_nop 1
	v_permlane32_swap_b32_e32 v164, v108

.LBB0_1318:
	ds_read_b128 v[2:5], v1
	ds_read_b128 v[18:21], v1 offset:4096
	ds_read_b128 v[134:137], v67
	ds_read_b128 v[228:231], v67 offset:4096
	ds_read_b128 v[232:235], v69
	ds_read_b128 v[236:239], v69 offset:4096
	ds_read_b128 v[240:243], v92
	ds_read_b128 v[244:247], v92 offset:4096
	s_waitcnt lgkmcnt(5)
	v_mfma_f32_32x32x16_bf16 v[2:17], v[62:65], v[2:5], 0
	v_mfma_f32_32x32x16_bf16 v[18:33], v[62:65], v[18:21], 0
	v_mfma_f32_32x32x16_bf16 v[2:17], v[58:61], v[134:137], v[2:17]
	s_waitcnt lgkmcnt(4)
	v_mfma_f32_32x32x16_bf16 v[18:33], v[58:61], v[228:231], v[18:33]
	s_waitcnt lgkmcnt(3)
	v_mfma_f32_32x32x16_bf16 v[2:17], v[54:57], v[232:235], v[2:17]
	s_waitcnt lgkmcnt(2)
	v_mfma_f32_32x32x16_bf16 v[18:33], v[54:57], v[236:239], v[18:33]
	s_waitcnt lgkmcnt(1)
	v_mfma_f32_32x32x16_bf16 v[2:17], v[50:53], v[240:243], v[2:17]
	s_waitcnt lgkmcnt(0)
	v_mfma_f32_32x32x16_bf16 v[18:33], v[50:53], v[244:247], v[18:33]
	s_nop 9
	v_max_i32_e32 v138, 0, v2
	v_max_i32_e32 v136, 0, v10
	v_max_i32_e32 v2, 0, v3
	v_max_i32_e32 v10, 0, v11
	v_max_i32_e32 v139, 0, v18
	v_pk_fma_f32 v[134:135], v[74:75], v[138:139], 0 op_sel_hi:[1,1,0]
	v_max_i32_e32 v137, 0, v26
	v_max_i32_e32 v3, 0, v19
	v_pk_fma_f32 v[136:137], v[76:77], v[136:137], 0 op_sel_hi:[1,1,0]
	v_pk_fma_f32 v[2:3], v[46:47], v[2:3], v[134:135]
	v_max_i32_e32 v11, 0, v27
	v_max_i32_e32 v18, 0, v4
	v_max_i32_e32 v19, 0, v20
	v_pk_fma_f32 v[10:11], v[42:43], v[10:11], v[136:137]
	v_pk_fma_f32 v[2:3], v[78:79], v[18:19], v[2:3]
	v_max_i32_e32 v18, 0, v12
	v_max_i32_e32 v19, 0, v28
	v_max_i32_e32 v4, 0, v5
	v_max_i32_e32 v5, 0, v21
	v_pk_fma_f32 v[10:11], v[80:81], v[18:19], v[10:11]
	v_pk_fma_f32 v[2:3], v[48:49], v[4:5], v[2:3]
	v_max_i32_e32 v4, 0, v13
	v_max_i32_e32 v5, 0, v29
	v_pk_fma_f32 v[4:5], v[44:45], v[4:5], v[10:11]
	v_max_i32_e32 v10, 0, v6
	v_max_i32_e32 v11, 0, v22
	v_pk_fma_f32 v[2:3], v[82:83], v[10:11], v[2:3]
	v_max_i32_e32 v10, 0, v14
	v_max_i32_e32 v11, 0, v30
	v_max_i32_e32 v6, 0, v7
	v_max_i32_e32 v7, 0, v23
	v_pk_fma_f32 v[4:5], v[84:85], v[10:11], v[4:5]
	v_pk_fma_f32 v[2:3], v[38:39], v[6:7], v[2:3]
	v_max_i32_e32 v6, 0, v15
	v_max_i32_e32 v7, 0, v31
	v_pk_fma_f32 v[4:5], v[34:35], v[6:7], v[4:5]
	v_max_i32_e32 v6, 0, v8
	v_max_i32_e32 v7, 0, v24
	v_pk_fma_f32 v[2:3], v[86:87], v[6:7], v[2:3]
	v_max_i32_e32 v6, 0, v16
	v_max_i32_e32 v7, 0, v32
	v_pk_fma_f32 v[4:5], v[88:89], v[6:7], v[4:5]
	v_max_i32_e32 v6, 0, v9
	v_max_i32_e32 v7, 0, v25
	v_pk_fma_f32 v[2:3], v[40:41], v[6:7], v[2:3]
	v_max_i32_e32 v6, 0, v17
	v_max_i32_e32 v7, 0, v33
	v_pk_fma_f32 v[4:5], v[36:37], v[6:7], v[4:5]
	v_not_b32_e32 v6, v2
	v_or_b32_e32 v7, 0x80000000, v2
	v_cmp_gt_i32_e32 vcc, 0, v2
	v_not_b32_e32 v2, v3
	s_nop 0
	v_cndmask_b32_e32 v206, v7, v6, vcc
	v_or_b32_e32 v6, 0x80000000, v3
	v_cmp_gt_i32_e32 vcc, 0, v3
	v_or_b32_e32 v3, 0x80000000, v4
	s_nop 0
	v_cndmask_b32_e32 v138, v6, v2, vcc
	v_not_b32_e32 v2, v4
	v_cmp_gt_i32_e32 vcc, 0, v4
	v_permlane32_swap_b32_e32 v206, v138
	s_nop 0
	v_cndmask_b32_e32 v170, v3, v2, vcc
	v_not_b32_e32 v2, v5
	v_or_b32_e32 v3, 0x80000000, v5
	v_cmp_gt_i32_e32 vcc, 0, v5
	s_nop 1
	v_cndmask_b32_e32 v109, v3, v2, vcc
	s_nop 1
	v_permlane32_swap_b32_e32 v170, v109

.LBB0_1344:
	ds_read_b128 v[2:5], v1 offset:8192
	ds_read_b128 v[18:21], v1 offset:12288
	ds_read_b128 v[134:137], v67 offset:8192
	ds_read_b128 v[228:231], v67 offset:12288
	ds_read_b128 v[232:235], v69 offset:8192
	ds_read_b128 v[236:239], v69 offset:12288
	ds_read_b128 v[240:243], v92 offset:8192
	ds_read_b128 v[244:247], v92 offset:12288
	s_waitcnt lgkmcnt(5)
	v_mfma_f32_32x32x16_bf16 v[2:17], v[62:65], v[2:5], 0
	v_mfma_f32_32x32x16_bf16 v[18:33], v[62:65], v[18:21], 0
	v_mfma_f32_32x32x16_bf16 v[2:17], v[58:61], v[134:137], v[2:17]
	s_waitcnt lgkmcnt(4)
	v_mfma_f32_32x32x16_bf16 v[18:33], v[58:61], v[228:231], v[18:33]
	s_waitcnt lgkmcnt(3)
	v_mfma_f32_32x32x16_bf16 v[2:17], v[54:57], v[232:235], v[2:17]
	s_waitcnt lgkmcnt(2)
	v_mfma_f32_32x32x16_bf16 v[18:33], v[54:57], v[236:239], v[18:33]
	s_waitcnt lgkmcnt(1)
	v_mfma_f32_32x32x16_bf16 v[2:17], v[50:53], v[240:243], v[2:17]
	s_waitcnt lgkmcnt(0)
	v_mfma_f32_32x32x16_bf16 v[18:33], v[50:53], v[244:247], v[18:33]
	s_nop 9
	v_max_i32_e32 v166, 0, v2
	v_max_i32_e32 v136, 0, v10
	v_max_i32_e32 v2, 0, v3
	v_max_i32_e32 v10, 0, v11
	v_max_i32_e32 v167, 0, v18
	v_pk_fma_f32 v[134:135], v[74:75], v[166:167], 0 op_sel_hi:[1,1,0]
	v_max_i32_e32 v137, 0, v26
	v_max_i32_e32 v3, 0, v19
	v_pk_fma_f32 v[136:137], v[76:77], v[136:137], 0 op_sel_hi:[1,1,0]
	v_pk_fma_f32 v[2:3], v[46:47], v[2:3], v[134:135]
	v_max_i32_e32 v11, 0, v27
	v_max_i32_e32 v18, 0, v4
	v_max_i32_e32 v19, 0, v20
	v_pk_fma_f32 v[10:11], v[42:43], v[10:11], v[136:137]
	v_pk_fma_f32 v[2:3], v[78:79], v[18:19], v[2:3]
	v_max_i32_e32 v18, 0, v12
	v_max_i32_e32 v19, 0, v28
	v_max_i32_e32 v4, 0, v5
	v_max_i32_e32 v5, 0, v21
	v_pk_fma_f32 v[10:11], v[80:81], v[18:19], v[10:11]
	v_pk_fma_f32 v[2:3], v[48:49], v[4:5], v[2:3]
	v_max_i32_e32 v4, 0, v13
	v_max_i32_e32 v5, 0, v29
	v_pk_fma_f32 v[4:5], v[44:45], v[4:5], v[10:11]
	v_max_i32_e32 v10, 0, v6
	v_max_i32_e32 v11, 0, v22
	v_pk_fma_f32 v[2:3], v[82:83], v[10:11], v[2:3]
	v_max_i32_e32 v10, 0, v14
	v_max_i32_e32 v11, 0, v30
	v_max_i32_e32 v6, 0, v7
	v_max_i32_e32 v7, 0, v23
	v_pk_fma_f32 v[4:5], v[84:85], v[10:11], v[4:5]
	v_pk_fma_f32 v[2:3], v[38:39], v[6:7], v[2:3]
	v_max_i32_e32 v6, 0, v15
	v_max_i32_e32 v7, 0, v31
	v_pk_fma_f32 v[4:5], v[34:35], v[6:7], v[4:5]
	v_max_i32_e32 v6, 0, v8
	v_max_i32_e32 v7, 0, v24
	v_pk_fma_f32 v[2:3], v[86:87], v[6:7], v[2:3]
	v_max_i32_e32 v6, 0, v16
	v_max_i32_e32 v7, 0, v32
	v_pk_fma_f32 v[4:5], v[88:89], v[6:7], v[4:5]
	v_max_i32_e32 v6, 0, v9
	v_max_i32_e32 v7, 0, v25
	v_pk_fma_f32 v[2:3], v[40:41], v[6:7], v[2:3]
	v_max_i32_e32 v6, 0, v17
	v_max_i32_e32 v7, 0, v33
	v_pk_fma_f32 v[4:5], v[36:37], v[6:7], v[4:5]
	v_not_b32_e32 v6, v2
	v_or_b32_e32 v7, 0x80000000, v2
	v_cmp_gt_i32_e32 vcc, 0, v2
	v_not_b32_e32 v2, v3
	s_nop 0
	v_cndmask_b32_e32 v207, v7, v6, vcc
	v_or_b32_e32 v6, 0x80000000, v3
	v_cmp_gt_i32_e32 vcc, 0, v3
	v_or_b32_e32 v3, 0x80000000, v4
	s_nop 0
	v_cndmask_b32_e32 v139, v6, v2, vcc
	v_not_b32_e32 v2, v4
	v_cmp_gt_i32_e32 vcc, 0, v4
	v_permlane32_swap_b32_e32 v207, v139
	s_nop 0
	v_cndmask_b32_e32 v171, v3, v2, vcc
	v_not_b32_e32 v2, v5
	v_or_b32_e32 v3, 0x80000000, v5
	v_cmp_gt_i32_e32 vcc, 0, v5
	s_nop 1
	v_cndmask_b32_e32 v110, v3, v2, vcc
	s_nop 1
	v_permlane32_swap_b32_e32 v171, v110

.LBB0_1370:
	ds_read_b128 v[2:5], v1 offset:16384
	ds_read_b128 v[18:21], v1 offset:20480
	ds_read_b128 v[134:137], v67 offset:16384
	ds_read_b128 v[228:231], v67 offset:20480
	ds_read_b128 v[232:235], v69 offset:16384
	ds_read_b128 v[236:239], v69 offset:20480
	ds_read_b128 v[240:243], v92 offset:16384
	ds_read_b128 v[244:247], v92 offset:20480
	s_waitcnt lgkmcnt(5)
	v_mfma_f32_32x32x16_bf16 v[2:17], v[62:65], v[2:5], 0
	v_mfma_f32_32x32x16_bf16 v[18:33], v[62:65], v[18:21], 0
	v_mfma_f32_32x32x16_bf16 v[2:17], v[58:61], v[134:137], v[2:17]
	s_waitcnt lgkmcnt(4)
	v_mfma_f32_32x32x16_bf16 v[18:33], v[58:61], v[228:231], v[18:33]
	s_waitcnt lgkmcnt(3)
	v_mfma_f32_32x32x16_bf16 v[2:17], v[54:57], v[232:235], v[2:17]
	s_waitcnt lgkmcnt(2)
	v_mfma_f32_32x32x16_bf16 v[18:33], v[54:57], v[236:239], v[18:33]
	s_waitcnt lgkmcnt(1)
	v_mfma_f32_32x32x16_bf16 v[2:17], v[50:53], v[240:243], v[2:17]
	s_waitcnt lgkmcnt(0)
	v_mfma_f32_32x32x16_bf16 v[18:33], v[50:53], v[244:247], v[18:33]
	s_nop 9
	v_max_i32_e32 v166, 0, v2
	v_max_i32_e32 v136, 0, v10
	v_max_i32_e32 v2, 0, v3
	v_max_i32_e32 v10, 0, v11
	v_max_i32_e32 v167, 0, v18
	v_pk_fma_f32 v[134:135], v[74:75], v[166:167], 0 op_sel_hi:[1,1,0]
	v_max_i32_e32 v137, 0, v26
	v_max_i32_e32 v3, 0, v19
	v_pk_fma_f32 v[136:137], v[76:77], v[136:137], 0 op_sel_hi:[1,1,0]
	v_pk_fma_f32 v[2:3], v[46:47], v[2:3], v[134:135]
	v_max_i32_e32 v11, 0, v27
	v_max_i32_e32 v18, 0, v4
	v_max_i32_e32 v19, 0, v20
	v_pk_fma_f32 v[10:11], v[42:43], v[10:11], v[136:137]
	v_pk_fma_f32 v[2:3], v[78:79], v[18:19], v[2:3]
	v_max_i32_e32 v18, 0, v12
	v_max_i32_e32 v19, 0, v28
	v_max_i32_e32 v4, 0, v5
	v_max_i32_e32 v5, 0, v21
	v_pk_fma_f32 v[10:11], v[80:81], v[18:19], v[10:11]
	v_pk_fma_f32 v[2:3], v[48:49], v[4:5], v[2:3]
	v_max_i32_e32 v4, 0, v13
	v_max_i32_e32 v5, 0, v29
	v_pk_fma_f32 v[4:5], v[44:45], v[4:5], v[10:11]
	v_max_i32_e32 v10, 0, v6
	v_max_i32_e32 v11, 0, v22
	v_pk_fma_f32 v[2:3], v[82:83], v[10:11], v[2:3]
	v_max_i32_e32 v10, 0, v14
	v_max_i32_e32 v11, 0, v30
	v_max_i32_e32 v6, 0, v7
	v_max_i32_e32 v7, 0, v23
	v_pk_fma_f32 v[4:5], v[84:85], v[10:11], v[4:5]
	v_pk_fma_f32 v[2:3], v[38:39], v[6:7], v[2:3]
	v_max_i32_e32 v6, 0, v15
	v_max_i32_e32 v7, 0, v31
	v_pk_fma_f32 v[4:5], v[34:35], v[6:7], v[4:5]
	v_max_i32_e32 v6, 0, v8
	v_max_i32_e32 v7, 0, v24
	v_pk_fma_f32 v[2:3], v[86:87], v[6:7], v[2:3]
	v_max_i32_e32 v6, 0, v16
	v_max_i32_e32 v7, 0, v32
	v_pk_fma_f32 v[4:5], v[88:89], v[6:7], v[4:5]
	v_max_i32_e32 v6, 0, v9
	v_max_i32_e32 v7, 0, v25
	v_pk_fma_f32 v[2:3], v[40:41], v[6:7], v[2:3]
	v_max_i32_e32 v6, 0, v17
	v_max_i32_e32 v7, 0, v33
	v_pk_fma_f32 v[4:5], v[36:37], v[6:7], v[4:5]
	v_not_b32_e32 v6, v2
	v_or_b32_e32 v7, 0x80000000, v2
	v_cmp_gt_i32_e32 vcc, 0, v2
	v_not_b32_e32 v2, v3
	s_nop 0
	v_cndmask_b32_e32 v208, v7, v6, vcc
	v_or_b32_e32 v6, 0x80000000, v3
	v_cmp_gt_i32_e32 vcc, 0, v3
	v_or_b32_e32 v3, 0x80000000, v4
	s_nop 0
	v_cndmask_b32_e32 v141, v6, v2, vcc
	v_not_b32_e32 v2, v4
	v_cmp_gt_i32_e32 vcc, 0, v4
	v_permlane32_swap_b32_e32 v208, v141
	s_nop 0
	v_cndmask_b32_e32 v173, v3, v2, vcc
	v_not_b32_e32 v2, v5
	v_or_b32_e32 v3, 0x80000000, v5
	v_cmp_gt_i32_e32 vcc, 0, v5
	s_nop 1
	v_cndmask_b32_e32 v112, v3, v2, vcc
	s_nop 1
	v_permlane32_swap_b32_e32 v173, v112

.LBB0_1396:
	ds_read_b128 v[2:5], v1 offset:24576
	ds_read_b128 v[18:21], v1 offset:28672
	ds_read_b128 v[134:137], v67 offset:24576
	ds_read_b128 v[228:231], v67 offset:28672
	ds_read_b128 v[232:235], v69 offset:24576
	ds_read_b128 v[236:239], v69 offset:28672
	ds_read_b128 v[240:243], v92 offset:24576
	ds_read_b128 v[244:247], v92 offset:28672
	s_waitcnt lgkmcnt(5)
	v_mfma_f32_32x32x16_bf16 v[2:17], v[62:65], v[2:5], 0
	v_mfma_f32_32x32x16_bf16 v[18:33], v[62:65], v[18:21], 0
	v_mfma_f32_32x32x16_bf16 v[2:17], v[58:61], v[134:137], v[2:17]
	s_waitcnt lgkmcnt(4)
	v_mfma_f32_32x32x16_bf16 v[18:33], v[58:61], v[228:231], v[18:33]
	s_waitcnt lgkmcnt(3)
	v_mfma_f32_32x32x16_bf16 v[2:17], v[54:57], v[232:235], v[2:17]
	s_waitcnt lgkmcnt(2)
	v_mfma_f32_32x32x16_bf16 v[18:33], v[54:57], v[236:239], v[18:33]
	s_waitcnt lgkmcnt(1)
	v_mfma_f32_32x32x16_bf16 v[2:17], v[50:53], v[240:243], v[2:17]
	s_waitcnt lgkmcnt(0)
	v_mfma_f32_32x32x16_bf16 v[18:33], v[50:53], v[244:247], v[18:33]
	s_nop 9
	v_max_i32_e32 v166, 0, v2
	v_max_i32_e32 v136, 0, v10
	v_max_i32_e32 v2, 0, v3
	v_max_i32_e32 v10, 0, v11
	v_max_i32_e32 v167, 0, v18
	v_pk_fma_f32 v[134:135], v[74:75], v[166:167], 0 op_sel_hi:[1,1,0]
	v_max_i32_e32 v137, 0, v26
	v_max_i32_e32 v3, 0, v19
	v_pk_fma_f32 v[136:137], v[76:77], v[136:137], 0 op_sel_hi:[1,1,0]
	v_pk_fma_f32 v[2:3], v[46:47], v[2:3], v[134:135]
	v_max_i32_e32 v11, 0, v27
	v_max_i32_e32 v18, 0, v4
	v_max_i32_e32 v19, 0, v20
	v_pk_fma_f32 v[10:11], v[42:43], v[10:11], v[136:137]
	v_pk_fma_f32 v[2:3], v[78:79], v[18:19], v[2:3]
	v_max_i32_e32 v18, 0, v12
	v_max_i32_e32 v19, 0, v28
	v_max_i32_e32 v4, 0, v5
	v_max_i32_e32 v5, 0, v21
	v_pk_fma_f32 v[10:11], v[80:81], v[18:19], v[10:11]
	v_pk_fma_f32 v[2:3], v[48:49], v[4:5], v[2:3]
	v_max_i32_e32 v4, 0, v13
	v_max_i32_e32 v5, 0, v29
	v_pk_fma_f32 v[4:5], v[44:45], v[4:5], v[10:11]
	v_max_i32_e32 v10, 0, v6
	v_max_i32_e32 v11, 0, v22
	v_pk_fma_f32 v[2:3], v[82:83], v[10:11], v[2:3]
	v_max_i32_e32 v10, 0, v14
	v_max_i32_e32 v11, 0, v30
	v_max_i32_e32 v6, 0, v7
	v_max_i32_e32 v7, 0, v23
	v_pk_fma_f32 v[4:5], v[84:85], v[10:11], v[4:5]
	v_pk_fma_f32 v[2:3], v[38:39], v[6:7], v[2:3]
	v_max_i32_e32 v6, 0, v15
	v_max_i32_e32 v7, 0, v31
	v_pk_fma_f32 v[4:5], v[34:35], v[6:7], v[4:5]
	v_max_i32_e32 v6, 0, v8
	v_max_i32_e32 v7, 0, v24
	v_pk_fma_f32 v[2:3], v[86:87], v[6:7], v[2:3]
	v_max_i32_e32 v6, 0, v16
	v_max_i32_e32 v7, 0, v32
	v_pk_fma_f32 v[4:5], v[88:89], v[6:7], v[4:5]
	v_max_i32_e32 v6, 0, v9
	v_max_i32_e32 v7, 0, v25
	v_pk_fma_f32 v[2:3], v[40:41], v[6:7], v[2:3]
	v_max_i32_e32 v6, 0, v17
	v_max_i32_e32 v7, 0, v33
	v_pk_fma_f32 v[4:5], v[36:37], v[6:7], v[4:5]
	v_not_b32_e32 v6, v2
	v_or_b32_e32 v7, 0x80000000, v2
	v_cmp_gt_i32_e32 vcc, 0, v2
	v_not_b32_e32 v2, v3
	s_nop 0
	v_cndmask_b32_e32 v209, v7, v6, vcc
	v_or_b32_e32 v6, 0x80000000, v3
	v_cmp_gt_i32_e32 vcc, 0, v3
	v_or_b32_e32 v3, 0x80000000, v4
	s_nop 0
	v_cndmask_b32_e32 v143, v6, v2, vcc
	v_not_b32_e32 v2, v4
	v_cmp_gt_i32_e32 vcc, 0, v4
	v_permlane32_swap_b32_e32 v209, v143
	s_nop 0
	v_cndmask_b32_e32 v180, v3, v2, vcc
	v_not_b32_e32 v2, v5
	v_or_b32_e32 v3, 0x80000000, v5
	v_cmp_gt_i32_e32 vcc, 0, v5
	s_nop 1
	v_cndmask_b32_e32 v114, v3, v2, vcc
	s_nop 1
	v_permlane32_swap_b32_e32 v180, v114

.LBB0_1422:
	ds_read_b128 v[2:5], v1 offset:32768
	ds_read_b128 v[18:21], v1 offset:36864
	ds_read_b128 v[134:137], v67 offset:32768
	ds_read_b128 v[228:231], v67 offset:36864
	ds_read_b128 v[232:235], v69 offset:32768
	ds_read_b128 v[236:239], v69 offset:36864
	ds_read_b128 v[240:243], v92 offset:32768
	ds_read_b128 v[244:247], v92 offset:36864
	s_waitcnt lgkmcnt(5)
	v_mfma_f32_32x32x16_bf16 v[2:17], v[62:65], v[2:5], 0
	v_mfma_f32_32x32x16_bf16 v[18:33], v[62:65], v[18:21], 0
	v_mfma_f32_32x32x16_bf16 v[2:17], v[58:61], v[134:137], v[2:17]
	s_waitcnt lgkmcnt(4)
	v_mfma_f32_32x32x16_bf16 v[18:33], v[58:61], v[228:231], v[18:33]
	s_waitcnt lgkmcnt(3)
	v_mfma_f32_32x32x16_bf16 v[2:17], v[54:57], v[232:235], v[2:17]
	s_waitcnt lgkmcnt(2)
	v_mfma_f32_32x32x16_bf16 v[18:33], v[54:57], v[236:239], v[18:33]
	s_waitcnt lgkmcnt(1)
	v_mfma_f32_32x32x16_bf16 v[2:17], v[50:53], v[240:243], v[2:17]
	s_waitcnt lgkmcnt(0)
	v_mfma_f32_32x32x16_bf16 v[18:33], v[50:53], v[244:247], v[18:33]
	s_nop 9
	v_max_i32_e32 v166, 0, v2
	v_max_i32_e32 v136, 0, v10
	v_max_i32_e32 v2, 0, v3
	v_max_i32_e32 v10, 0, v11
	v_max_i32_e32 v167, 0, v18
	v_pk_fma_f32 v[134:135], v[74:75], v[166:167], 0 op_sel_hi:[1,1,0]
	v_max_i32_e32 v137, 0, v26
	v_max_i32_e32 v3, 0, v19
	v_pk_fma_f32 v[136:137], v[76:77], v[136:137], 0 op_sel_hi:[1,1,0]
	v_pk_fma_f32 v[2:3], v[46:47], v[2:3], v[134:135]
	v_max_i32_e32 v11, 0, v27
	v_max_i32_e32 v18, 0, v4
	v_max_i32_e32 v19, 0, v20
	v_pk_fma_f32 v[10:11], v[42:43], v[10:11], v[136:137]
	v_pk_fma_f32 v[2:3], v[78:79], v[18:19], v[2:3]
	v_max_i32_e32 v18, 0, v12
	v_max_i32_e32 v19, 0, v28
	v_max_i32_e32 v4, 0, v5
	v_max_i32_e32 v5, 0, v21
	v_pk_fma_f32 v[10:11], v[80:81], v[18:19], v[10:11]
	v_pk_fma_f32 v[2:3], v[48:49], v[4:5], v[2:3]
	v_max_i32_e32 v4, 0, v13
	v_max_i32_e32 v5, 0, v29
	v_pk_fma_f32 v[4:5], v[44:45], v[4:5], v[10:11]
	v_max_i32_e32 v10, 0, v6
	v_max_i32_e32 v11, 0, v22
	v_pk_fma_f32 v[2:3], v[82:83], v[10:11], v[2:3]
	v_max_i32_e32 v10, 0, v14
	v_max_i32_e32 v11, 0, v30
	v_max_i32_e32 v6, 0, v7
	v_max_i32_e32 v7, 0, v23
	v_pk_fma_f32 v[4:5], v[84:85], v[10:11], v[4:5]
	v_pk_fma_f32 v[2:3], v[38:39], v[6:7], v[2:3]
	v_max_i32_e32 v6, 0, v15
	v_max_i32_e32 v7, 0, v31
	v_pk_fma_f32 v[4:5], v[34:35], v[6:7], v[4:5]
	v_max_i32_e32 v6, 0, v8
	v_max_i32_e32 v7, 0, v24
	v_pk_fma_f32 v[2:3], v[86:87], v[6:7], v[2:3]
	v_max_i32_e32 v6, 0, v16
	v_max_i32_e32 v7, 0, v32
	v_pk_fma_f32 v[4:5], v[88:89], v[6:7], v[4:5]
	v_max_i32_e32 v6, 0, v9
	v_max_i32_e32 v7, 0, v25
	v_pk_fma_f32 v[2:3], v[40:41], v[6:7], v[2:3]
	v_max_i32_e32 v6, 0, v17
	v_max_i32_e32 v7, 0, v33
	v_pk_fma_f32 v[4:5], v[36:37], v[6:7], v[4:5]
	v_not_b32_e32 v6, v2
	v_or_b32_e32 v7, 0x80000000, v2
	v_cmp_gt_i32_e32 vcc, 0, v2
	v_not_b32_e32 v2, v3
	s_nop 0
	v_cndmask_b32_e32 v210, v7, v6, vcc
	v_or_b32_e32 v6, 0x80000000, v3
	v_cmp_gt_i32_e32 vcc, 0, v3
	v_or_b32_e32 v3, 0x80000000, v4
	s_nop 0
	v_cndmask_b32_e32 v145, v6, v2, vcc
	v_not_b32_e32 v2, v4
	v_cmp_gt_i32_e32 vcc, 0, v4
	v_permlane32_swap_b32_e32 v210, v145
	s_nop 0
	v_cndmask_b32_e32 v182, v3, v2, vcc
	v_not_b32_e32 v2, v5
	v_or_b32_e32 v3, 0x80000000, v5
	v_cmp_gt_i32_e32 vcc, 0, v5
	s_nop 1
	v_cndmask_b32_e32 v116, v3, v2, vcc
	s_nop 1
	v_permlane32_swap_b32_e32 v182, v116

.LBB0_1448:
	ds_read_b128 v[2:5], v1 offset:40960
	ds_read_b128 v[18:21], v1 offset:45056
	ds_read_b128 v[134:137], v67 offset:40960
	ds_read_b128 v[228:231], v67 offset:45056
	ds_read_b128 v[232:235], v69 offset:40960
	ds_read_b128 v[236:239], v69 offset:45056
	ds_read_b128 v[240:243], v92 offset:40960
	ds_read_b128 v[244:247], v92 offset:45056
	s_waitcnt lgkmcnt(5)
	v_mfma_f32_32x32x16_bf16 v[2:17], v[62:65], v[2:5], 0
	v_mfma_f32_32x32x16_bf16 v[18:33], v[62:65], v[18:21], 0
	v_mfma_f32_32x32x16_bf16 v[2:17], v[58:61], v[134:137], v[2:17]
	s_waitcnt lgkmcnt(4)
	v_mfma_f32_32x32x16_bf16 v[18:33], v[58:61], v[228:231], v[18:33]
	s_waitcnt lgkmcnt(3)
	v_mfma_f32_32x32x16_bf16 v[2:17], v[54:57], v[232:235], v[2:17]
	s_waitcnt lgkmcnt(2)
	v_mfma_f32_32x32x16_bf16 v[18:33], v[54:57], v[236:239], v[18:33]
	s_waitcnt lgkmcnt(1)
	v_mfma_f32_32x32x16_bf16 v[2:17], v[50:53], v[240:243], v[2:17]
	s_waitcnt lgkmcnt(0)
	v_mfma_f32_32x32x16_bf16 v[18:33], v[50:53], v[244:247], v[18:33]
	s_nop 9
	v_max_i32_e32 v166, 0, v2
	v_max_i32_e32 v136, 0, v10
	v_max_i32_e32 v2, 0, v3
	v_max_i32_e32 v10, 0, v11
	v_max_i32_e32 v167, 0, v18
	v_pk_fma_f32 v[134:135], v[74:75], v[166:167], 0 op_sel_hi:[1,1,0]
	v_max_i32_e32 v137, 0, v26
	v_max_i32_e32 v3, 0, v19
	v_pk_fma_f32 v[136:137], v[76:77], v[136:137], 0 op_sel_hi:[1,1,0]
	v_pk_fma_f32 v[2:3], v[46:47], v[2:3], v[134:135]
	v_max_i32_e32 v11, 0, v27
	v_max_i32_e32 v18, 0, v4
	v_max_i32_e32 v19, 0, v20
	v_pk_fma_f32 v[10:11], v[42:43], v[10:11], v[136:137]
	v_pk_fma_f32 v[2:3], v[78:79], v[18:19], v[2:3]
	v_max_i32_e32 v18, 0, v12
	v_max_i32_e32 v19, 0, v28
	v_max_i32_e32 v4, 0, v5
	v_max_i32_e32 v5, 0, v21
	v_pk_fma_f32 v[10:11], v[80:81], v[18:19], v[10:11]
	v_pk_fma_f32 v[2:3], v[48:49], v[4:5], v[2:3]
	v_max_i32_e32 v4, 0, v13
	v_max_i32_e32 v5, 0, v29
	v_pk_fma_f32 v[4:5], v[44:45], v[4:5], v[10:11]
	v_max_i32_e32 v10, 0, v6
	v_max_i32_e32 v11, 0, v22
	v_pk_fma_f32 v[2:3], v[82:83], v[10:11], v[2:3]
	v_max_i32_e32 v10, 0, v14
	v_max_i32_e32 v11, 0, v30
	v_max_i32_e32 v6, 0, v7
	v_max_i32_e32 v7, 0, v23
	v_pk_fma_f32 v[4:5], v[84:85], v[10:11], v[4:5]
	v_pk_fma_f32 v[2:3], v[38:39], v[6:7], v[2:3]
	v_max_i32_e32 v6, 0, v15
	v_max_i32_e32 v7, 0, v31
	v_pk_fma_f32 v[4:5], v[34:35], v[6:7], v[4:5]
	v_max_i32_e32 v6, 0, v8
	v_max_i32_e32 v7, 0, v24
	v_pk_fma_f32 v[2:3], v[86:87], v[6:7], v[2:3]
	v_max_i32_e32 v6, 0, v16
	v_max_i32_e32 v7, 0, v32
	v_pk_fma_f32 v[4:5], v[88:89], v[6:7], v[4:5]
	v_max_i32_e32 v6, 0, v9
	v_max_i32_e32 v7, 0, v25
	v_pk_fma_f32 v[2:3], v[40:41], v[6:7], v[2:3]
	v_max_i32_e32 v6, 0, v17
	v_max_i32_e32 v7, 0, v33
	v_pk_fma_f32 v[4:5], v[36:37], v[6:7], v[4:5]
	v_not_b32_e32 v6, v2
	v_or_b32_e32 v7, 0x80000000, v2
	v_cmp_gt_i32_e32 vcc, 0, v2
	v_not_b32_e32 v2, v3
	s_nop 0
	v_cndmask_b32_e32 v211, v7, v6, vcc
	v_or_b32_e32 v6, 0x80000000, v3
	v_cmp_gt_i32_e32 vcc, 0, v3
	v_or_b32_e32 v3, 0x80000000, v4
	s_nop 0
	v_cndmask_b32_e32 v147, v6, v2, vcc
	v_not_b32_e32 v2, v4
	v_cmp_gt_i32_e32 vcc, 0, v4
	v_permlane32_swap_b32_e32 v211, v147
	s_nop 0
	v_cndmask_b32_e32 v184, v3, v2, vcc
	v_not_b32_e32 v2, v5
	v_or_b32_e32 v3, 0x80000000, v5
	v_cmp_gt_i32_e32 vcc, 0, v5
	s_nop 1
	v_cndmask_b32_e32 v118, v3, v2, vcc
	s_nop 1
	v_permlane32_swap_b32_e32 v184, v118

.LBB0_1474:
	ds_read_b128 v[2:5], v1 offset:49152
	ds_read_b128 v[18:21], v1 offset:53248
	ds_read_b128 v[134:137], v67 offset:49152
	ds_read_b128 v[228:231], v67 offset:53248
	ds_read_b128 v[232:235], v69 offset:49152
	ds_read_b128 v[236:239], v69 offset:53248
	ds_read_b128 v[240:243], v92 offset:49152
	ds_read_b128 v[244:247], v92 offset:53248
	s_waitcnt lgkmcnt(5)
	v_mfma_f32_32x32x16_bf16 v[2:17], v[62:65], v[2:5], 0
	v_mfma_f32_32x32x16_bf16 v[18:33], v[62:65], v[18:21], 0
	v_mfma_f32_32x32x16_bf16 v[2:17], v[58:61], v[134:137], v[2:17]
	s_waitcnt lgkmcnt(4)
	v_mfma_f32_32x32x16_bf16 v[18:33], v[58:61], v[228:231], v[18:33]
	s_waitcnt lgkmcnt(3)
	v_mfma_f32_32x32x16_bf16 v[2:17], v[54:57], v[232:235], v[2:17]
	s_waitcnt lgkmcnt(2)
	v_mfma_f32_32x32x16_bf16 v[18:33], v[54:57], v[236:239], v[18:33]
	s_waitcnt lgkmcnt(1)
	v_mfma_f32_32x32x16_bf16 v[2:17], v[50:53], v[240:243], v[2:17]
	s_waitcnt lgkmcnt(0)
	v_mfma_f32_32x32x16_bf16 v[18:33], v[50:53], v[244:247], v[18:33]
	s_nop 9
	v_max_i32_e32 v166, 0, v2
	v_max_i32_e32 v136, 0, v10
	v_max_i32_e32 v2, 0, v3
	v_max_i32_e32 v10, 0, v11
	v_max_i32_e32 v167, 0, v18
	v_pk_fma_f32 v[134:135], v[74:75], v[166:167], 0 op_sel_hi:[1,1,0]
	v_max_i32_e32 v137, 0, v26
	v_max_i32_e32 v3, 0, v19
	v_pk_fma_f32 v[136:137], v[76:77], v[136:137], 0 op_sel_hi:[1,1,0]
	v_pk_fma_f32 v[2:3], v[46:47], v[2:3], v[134:135]
	v_max_i32_e32 v11, 0, v27
	v_max_i32_e32 v18, 0, v4
	v_max_i32_e32 v19, 0, v20
	v_pk_fma_f32 v[10:11], v[42:43], v[10:11], v[136:137]
	v_pk_fma_f32 v[2:3], v[78:79], v[18:19], v[2:3]
	v_max_i32_e32 v18, 0, v12
	v_max_i32_e32 v19, 0, v28
	v_max_i32_e32 v4, 0, v5
	v_max_i32_e32 v5, 0, v21
	v_pk_fma_f32 v[10:11], v[80:81], v[18:19], v[10:11]
	v_pk_fma_f32 v[2:3], v[48:49], v[4:5], v[2:3]
	v_max_i32_e32 v4, 0, v13
	v_max_i32_e32 v5, 0, v29
	v_pk_fma_f32 v[4:5], v[44:45], v[4:5], v[10:11]
	v_max_i32_e32 v10, 0, v6
	v_max_i32_e32 v11, 0, v22
	v_pk_fma_f32 v[2:3], v[82:83], v[10:11], v[2:3]
	v_max_i32_e32 v10, 0, v14
	v_max_i32_e32 v11, 0, v30
	v_max_i32_e32 v6, 0, v7
	v_max_i32_e32 v7, 0, v23
	v_pk_fma_f32 v[4:5], v[84:85], v[10:11], v[4:5]
	v_pk_fma_f32 v[2:3], v[38:39], v[6:7], v[2:3]
	v_max_i32_e32 v6, 0, v15
	v_max_i32_e32 v7, 0, v31
	v_pk_fma_f32 v[4:5], v[34:35], v[6:7], v[4:5]
	v_max_i32_e32 v6, 0, v8
	v_max_i32_e32 v7, 0, v24
	v_pk_fma_f32 v[2:3], v[86:87], v[6:7], v[2:3]
	v_max_i32_e32 v6, 0, v16
	v_max_i32_e32 v7, 0, v32
	v_pk_fma_f32 v[4:5], v[88:89], v[6:7], v[4:5]
	v_max_i32_e32 v6, 0, v9
	v_max_i32_e32 v7, 0, v25
	v_pk_fma_f32 v[2:3], v[40:41], v[6:7], v[2:3]
	v_max_i32_e32 v6, 0, v17
	v_max_i32_e32 v7, 0, v33
	v_pk_fma_f32 v[4:5], v[36:37], v[6:7], v[4:5]
	v_not_b32_e32 v6, v2
	v_or_b32_e32 v7, 0x80000000, v2
	v_cmp_gt_i32_e32 vcc, 0, v2
	v_not_b32_e32 v2, v3
	s_nop 0
	v_cndmask_b32_e32 v212, v7, v6, vcc
	v_or_b32_e32 v6, 0x80000000, v3
	v_cmp_gt_i32_e32 vcc, 0, v3
	v_or_b32_e32 v3, 0x80000000, v4
	s_nop 0
	v_cndmask_b32_e32 v149, v6, v2, vcc
	v_not_b32_e32 v2, v4
	v_cmp_gt_i32_e32 vcc, 0, v4
	v_permlane32_swap_b32_e32 v212, v149
	s_nop 0
	v_cndmask_b32_e32 v186, v3, v2, vcc
	v_not_b32_e32 v2, v5
	v_or_b32_e32 v3, 0x80000000, v5
	v_cmp_gt_i32_e32 vcc, 0, v5
	s_nop 1
	v_cndmask_b32_e32 v120, v3, v2, vcc
	s_nop 1
	v_permlane32_swap_b32_e32 v186, v120

.LBB0_1500:
	ds_read_b128 v[2:5], v1 offset:57344
	ds_read_b128 v[18:21], v1 offset:61440
	ds_read_b128 v[134:137], v67 offset:57344
	ds_read_b128 v[228:231], v67 offset:61440
	ds_read_b128 v[232:235], v69 offset:57344
	ds_read_b128 v[236:239], v69 offset:61440
	ds_read_b128 v[240:243], v92 offset:57344
	ds_read_b128 v[244:247], v92 offset:61440
	s_waitcnt lgkmcnt(5)
	v_mfma_f32_32x32x16_bf16 v[2:17], v[62:65], v[2:5], 0
	v_mfma_f32_32x32x16_bf16 v[18:33], v[62:65], v[18:21], 0
	v_mfma_f32_32x32x16_bf16 v[2:17], v[58:61], v[134:137], v[2:17]
	s_waitcnt lgkmcnt(4)
	v_mfma_f32_32x32x16_bf16 v[18:33], v[58:61], v[228:231], v[18:33]
	s_waitcnt lgkmcnt(3)
	v_mfma_f32_32x32x16_bf16 v[2:17], v[54:57], v[232:235], v[2:17]
	s_waitcnt lgkmcnt(2)
	v_mfma_f32_32x32x16_bf16 v[18:33], v[54:57], v[236:239], v[18:33]
	s_waitcnt lgkmcnt(1)
	v_mfma_f32_32x32x16_bf16 v[2:17], v[50:53], v[240:243], v[2:17]
	s_waitcnt lgkmcnt(0)
	v_mfma_f32_32x32x16_bf16 v[18:33], v[50:53], v[244:247], v[18:33]
	s_nop 9
	v_max_i32_e32 v166, 0, v2
	v_max_i32_e32 v136, 0, v10
	v_max_i32_e32 v2, 0, v3
	v_max_i32_e32 v10, 0, v11
	v_max_i32_e32 v167, 0, v18
	v_pk_fma_f32 v[134:135], v[74:75], v[166:167], 0 op_sel_hi:[1,1,0]
	v_max_i32_e32 v137, 0, v26
	v_max_i32_e32 v3, 0, v19
	v_pk_fma_f32 v[136:137], v[76:77], v[136:137], 0 op_sel_hi:[1,1,0]
	v_pk_fma_f32 v[2:3], v[46:47], v[2:3], v[134:135]
	v_max_i32_e32 v11, 0, v27
	v_max_i32_e32 v18, 0, v4
	v_max_i32_e32 v19, 0, v20
	v_pk_fma_f32 v[10:11], v[42:43], v[10:11], v[136:137]
	v_pk_fma_f32 v[2:3], v[78:79], v[18:19], v[2:3]
	v_max_i32_e32 v18, 0, v12
	v_max_i32_e32 v19, 0, v28
	v_max_i32_e32 v4, 0, v5
	v_max_i32_e32 v5, 0, v21
	v_pk_fma_f32 v[10:11], v[80:81], v[18:19], v[10:11]
	v_pk_fma_f32 v[2:3], v[48:49], v[4:5], v[2:3]
	v_max_i32_e32 v4, 0, v13
	v_max_i32_e32 v5, 0, v29
	v_pk_fma_f32 v[4:5], v[44:45], v[4:5], v[10:11]
	v_max_i32_e32 v10, 0, v6
	v_max_i32_e32 v11, 0, v22
	v_pk_fma_f32 v[2:3], v[82:83], v[10:11], v[2:3]
	v_max_i32_e32 v10, 0, v14
	v_max_i32_e32 v11, 0, v30
	v_max_i32_e32 v6, 0, v7
	v_max_i32_e32 v7, 0, v23
	v_pk_fma_f32 v[4:5], v[84:85], v[10:11], v[4:5]
	v_pk_fma_f32 v[2:3], v[38:39], v[6:7], v[2:3]
	v_max_i32_e32 v6, 0, v15
	v_max_i32_e32 v7, 0, v31
	v_pk_fma_f32 v[4:5], v[34:35], v[6:7], v[4:5]
	v_max_i32_e32 v6, 0, v8
	v_max_i32_e32 v7, 0, v24
	v_pk_fma_f32 v[2:3], v[86:87], v[6:7], v[2:3]
	v_max_i32_e32 v6, 0, v16
	v_max_i32_e32 v7, 0, v32
	v_pk_fma_f32 v[4:5], v[88:89], v[6:7], v[4:5]
	v_max_i32_e32 v6, 0, v9
	v_max_i32_e32 v7, 0, v25
	v_pk_fma_f32 v[2:3], v[40:41], v[6:7], v[2:3]
	v_max_i32_e32 v6, 0, v17
	v_max_i32_e32 v7, 0, v33
	v_pk_fma_f32 v[4:5], v[36:37], v[6:7], v[4:5]
	v_not_b32_e32 v6, v2
	v_or_b32_e32 v7, 0x80000000, v2
	v_cmp_gt_i32_e32 vcc, 0, v2
	v_not_b32_e32 v2, v3
	s_nop 0
	v_cndmask_b32_e32 v213, v7, v6, vcc
	v_or_b32_e32 v6, 0x80000000, v3
	v_cmp_gt_i32_e32 vcc, 0, v3
	v_or_b32_e32 v3, 0x80000000, v4
	s_nop 0
	v_cndmask_b32_e32 v151, v6, v2, vcc
	v_not_b32_e32 v2, v4
	v_cmp_gt_i32_e32 vcc, 0, v4
	v_permlane32_swap_b32_e32 v213, v151
	s_nop 0
	v_cndmask_b32_e32 v188, v3, v2, vcc
	v_not_b32_e32 v2, v5
	v_or_b32_e32 v3, 0x80000000, v5
	v_cmp_gt_i32_e32 vcc, 0, v5
	s_nop 1
	v_cndmask_b32_e32 v122, v3, v2, vcc
	s_nop 1
	v_permlane32_swap_b32_e32 v188, v122

.LBB0_1526:
	ds_read_b128 v[2:5], v1
	ds_read_b128 v[18:21], v1 offset:4096
	ds_read_b128 v[134:137], v67
	ds_read_b128 v[228:231], v67 offset:4096
	ds_read_b128 v[232:235], v69
	ds_read_b128 v[236:239], v69 offset:4096
	ds_read_b128 v[240:243], v92
	ds_read_b128 v[244:247], v92 offset:4096
	s_waitcnt lgkmcnt(5)
	v_mfma_f32_32x32x16_bf16 v[2:17], v[62:65], v[2:5], 0
	v_mfma_f32_32x32x16_bf16 v[18:33], v[62:65], v[18:21], 0
	v_mfma_f32_32x32x16_bf16 v[2:17], v[58:61], v[134:137], v[2:17]
	s_waitcnt lgkmcnt(4)
	v_mfma_f32_32x32x16_bf16 v[18:33], v[58:61], v[228:231], v[18:33]
	s_waitcnt lgkmcnt(3)
	v_mfma_f32_32x32x16_bf16 v[2:17], v[54:57], v[232:235], v[2:17]
	s_waitcnt lgkmcnt(2)
	v_mfma_f32_32x32x16_bf16 v[18:33], v[54:57], v[236:239], v[18:33]
	s_waitcnt lgkmcnt(1)
	v_mfma_f32_32x32x16_bf16 v[2:17], v[50:53], v[240:243], v[2:17]
	s_waitcnt lgkmcnt(0)
	v_mfma_f32_32x32x16_bf16 v[18:33], v[50:53], v[244:247], v[18:33]
	s_nop 9
	v_max_i32_e32 v90, 0, v2
	v_max_i32_e32 v134, 0, v10
	v_max_i32_e32 v2, 0, v3
	v_max_i32_e32 v10, 0, v11
	v_max_i32_e32 v91, 0, v18
	v_pk_fma_f32 v[90:91], v[74:75], v[90:91], 0 op_sel_hi:[1,1,0]
	v_max_i32_e32 v135, 0, v26
	v_max_i32_e32 v3, 0, v19
	v_pk_fma_f32 v[134:135], v[76:77], v[134:135], 0 op_sel_hi:[1,1,0]
	v_pk_fma_f32 v[2:3], v[46:47], v[2:3], v[90:91]
	v_max_i32_e32 v11, 0, v27
	v_max_i32_e32 v18, 0, v4
	v_max_i32_e32 v19, 0, v20
	v_pk_fma_f32 v[10:11], v[42:43], v[10:11], v[134:135]
	v_pk_fma_f32 v[2:3], v[78:79], v[18:19], v[2:3]
	v_max_i32_e32 v18, 0, v12
	v_max_i32_e32 v19, 0, v28
	v_max_i32_e32 v4, 0, v5
	v_max_i32_e32 v5, 0, v21
	v_pk_fma_f32 v[10:11], v[80:81], v[18:19], v[10:11]
	v_pk_fma_f32 v[2:3], v[48:49], v[4:5], v[2:3]
	v_max_i32_e32 v4, 0, v13
	v_max_i32_e32 v5, 0, v29
	v_pk_fma_f32 v[4:5], v[44:45], v[4:5], v[10:11]
	v_max_i32_e32 v10, 0, v6
	v_max_i32_e32 v11, 0, v22
	v_pk_fma_f32 v[2:3], v[82:83], v[10:11], v[2:3]
	v_max_i32_e32 v10, 0, v14
	v_max_i32_e32 v11, 0, v30
	v_max_i32_e32 v6, 0, v7
	v_max_i32_e32 v7, 0, v23
	v_pk_fma_f32 v[4:5], v[84:85], v[10:11], v[4:5]
	v_pk_fma_f32 v[2:3], v[38:39], v[6:7], v[2:3]
	v_max_i32_e32 v6, 0, v15
	v_max_i32_e32 v7, 0, v31
	v_pk_fma_f32 v[4:5], v[34:35], v[6:7], v[4:5]
	v_max_i32_e32 v6, 0, v8
	v_max_i32_e32 v7, 0, v24
	v_pk_fma_f32 v[2:3], v[86:87], v[6:7], v[2:3]
	v_max_i32_e32 v6, 0, v16
	v_max_i32_e32 v7, 0, v32
	v_pk_fma_f32 v[4:5], v[88:89], v[6:7], v[4:5]
	v_max_i32_e32 v6, 0, v9
	v_max_i32_e32 v7, 0, v25
	v_pk_fma_f32 v[2:3], v[40:41], v[6:7], v[2:3]
	v_max_i32_e32 v6, 0, v17
	v_max_i32_e32 v7, 0, v33
	v_pk_fma_f32 v[4:5], v[36:37], v[6:7], v[4:5]
	v_not_b32_e32 v6, v2
	v_or_b32_e32 v7, 0x80000000, v2
	v_cmp_gt_i32_e32 vcc, 0, v2
	v_not_b32_e32 v2, v3
	s_nop 0
	v_cndmask_b32_e32 v214, v7, v6, vcc
	v_or_b32_e32 v6, 0x80000000, v3
	v_cmp_gt_i32_e32 vcc, 0, v3
	v_or_b32_e32 v3, 0x80000000, v4
	s_nop 0
	v_cndmask_b32_e32 v160, v6, v2, vcc
	v_not_b32_e32 v2, v4
	v_cmp_gt_i32_e32 vcc, 0, v4
	v_permlane32_swap_b32_e32 v214, v160
	s_nop 0
	v_cndmask_b32_e32 v197, v3, v2, vcc
	v_not_b32_e32 v2, v5
	v_or_b32_e32 v3, 0x80000000, v5
	v_cmp_gt_i32_e32 vcc, 0, v5
	s_nop 1
	v_cndmask_b32_e32 v131, v3, v2, vcc
	s_nop 1
	v_permlane32_swap_b32_e32 v197, v131

.LBB0_1550:
	s_barrier
	ds_read_b128 v[2:5], v1 offset:8192
	ds_read_b128 v[18:21], v1 offset:12288
	ds_read_b128 v[134:137], v67 offset:8192
	ds_read_b128 v[228:231], v67 offset:12288
	ds_read_b128 v[232:235], v69 offset:8192
	ds_read_b128 v[236:239], v69 offset:12288
	ds_read_b128 v[240:243], v92 offset:8192
	ds_read_b128 v[244:247], v92 offset:12288
	s_waitcnt lgkmcnt(5)
	v_mfma_f32_32x32x16_bf16 v[2:17], v[62:65], v[2:5], 0
	v_mfma_f32_32x32x16_bf16 v[18:33], v[62:65], v[18:21], 0
	v_mfma_f32_32x32x16_bf16 v[2:17], v[58:61], v[134:137], v[2:17]
	s_waitcnt lgkmcnt(4)
	v_mfma_f32_32x32x16_bf16 v[18:33], v[58:61], v[228:231], v[18:33]
	s_waitcnt lgkmcnt(3)
	v_mfma_f32_32x32x16_bf16 v[2:17], v[54:57], v[232:235], v[2:17]
	s_waitcnt lgkmcnt(2)
	v_mfma_f32_32x32x16_bf16 v[18:33], v[54:57], v[236:239], v[18:33]
	s_waitcnt lgkmcnt(1)
	v_mfma_f32_32x32x16_bf16 v[2:17], v[50:53], v[240:243], v[2:17]
	s_waitcnt lgkmcnt(0)
	v_mfma_f32_32x32x16_bf16 v[18:33], v[50:53], v[244:247], v[18:33]
	s_nop 9
	v_max_i32_e32 v90, 0, v2
	v_max_i32_e32 v134, 0, v10
	v_max_i32_e32 v2, 0, v3
	v_max_i32_e32 v10, 0, v11
	v_max_i32_e32 v91, 0, v18
	v_pk_fma_f32 v[90:91], v[74:75], v[90:91], 0 op_sel_hi:[1,1,0]
	v_max_i32_e32 v135, 0, v26
	v_max_i32_e32 v3, 0, v19
	v_pk_fma_f32 v[134:135], v[76:77], v[134:135], 0 op_sel_hi:[1,1,0]
	v_pk_fma_f32 v[2:3], v[46:47], v[2:3], v[90:91]
	v_max_i32_e32 v11, 0, v27
	v_max_i32_e32 v18, 0, v4
	v_max_i32_e32 v19, 0, v20
	v_pk_fma_f32 v[10:11], v[42:43], v[10:11], v[134:135]
	v_pk_fma_f32 v[2:3], v[78:79], v[18:19], v[2:3]
	v_max_i32_e32 v18, 0, v12
	v_max_i32_e32 v19, 0, v28
	v_max_i32_e32 v4, 0, v5
	v_max_i32_e32 v5, 0, v21
	v_pk_fma_f32 v[10:11], v[80:81], v[18:19], v[10:11]
	v_pk_fma_f32 v[2:3], v[48:49], v[4:5], v[2:3]
	v_max_i32_e32 v4, 0, v13
	v_max_i32_e32 v5, 0, v29
	v_pk_fma_f32 v[4:5], v[44:45], v[4:5], v[10:11]
	v_max_i32_e32 v10, 0, v6
	v_max_i32_e32 v11, 0, v22
	v_pk_fma_f32 v[2:3], v[82:83], v[10:11], v[2:3]
	v_max_i32_e32 v10, 0, v14
	v_max_i32_e32 v11, 0, v30
	v_max_i32_e32 v6, 0, v7
	v_max_i32_e32 v7, 0, v23
	v_pk_fma_f32 v[4:5], v[84:85], v[10:11], v[4:5]
	v_pk_fma_f32 v[2:3], v[38:39], v[6:7], v[2:3]
	v_max_i32_e32 v6, 0, v15
	v_max_i32_e32 v7, 0, v31
	v_pk_fma_f32 v[4:5], v[34:35], v[6:7], v[4:5]
	v_max_i32_e32 v6, 0, v8
	v_max_i32_e32 v7, 0, v24
	v_pk_fma_f32 v[2:3], v[86:87], v[6:7], v[2:3]
	v_max_i32_e32 v6, 0, v16
	v_max_i32_e32 v7, 0, v32
	v_pk_fma_f32 v[4:5], v[88:89], v[6:7], v[4:5]
	v_max_i32_e32 v6, 0, v9
	v_max_i32_e32 v7, 0, v25
	v_pk_fma_f32 v[2:3], v[40:41], v[6:7], v[2:3]
	v_max_i32_e32 v6, 0, v17
	v_max_i32_e32 v7, 0, v33
	v_pk_fma_f32 v[4:5], v[36:37], v[6:7], v[4:5]
	v_not_b32_e32 v6, v2
	v_or_b32_e32 v7, 0x80000000, v2
	v_cmp_gt_i32_e32 vcc, 0, v2
	v_not_b32_e32 v2, v3
	s_nop 0
	v_cndmask_b32_e32 v215, v7, v6, vcc
	v_or_b32_e32 v6, 0x80000000, v3
	v_cmp_gt_i32_e32 vcc, 0, v3
	v_or_b32_e32 v3, 0x80000000, v4
	s_nop 0
	v_cndmask_b32_e32 v163, v6, v2, vcc
	v_not_b32_e32 v2, v4
	v_cmp_gt_i32_e32 vcc, 0, v4
	v_permlane32_swap_b32_e32 v215, v163
	s_nop 0
	v_cndmask_b32_e32 v199, v3, v2, vcc
	v_not_b32_e32 v2, v5
	v_or_b32_e32 v3, 0x80000000, v5
	v_cmp_gt_i32_e32 vcc, 0, v5
	s_nop 1
	v_cndmask_b32_e32 v90, v3, v2, vcc
	s_nop 1
	v_permlane32_swap_b32_e32 v199, v90

.LBB0_1570:
	s_barrier
	ds_read_b128 v[2:5], v1 offset:16384
	ds_read_b128 v[18:21], v1 offset:20480
	ds_read_b128 v[134:137], v67 offset:16384
	ds_read_b128 v[228:231], v67 offset:20480
	ds_read_b128 v[232:235], v69 offset:16384
	ds_read_b128 v[236:239], v69 offset:20480
	ds_read_b128 v[240:243], v92 offset:16384
	ds_read_b128 v[244:247], v92 offset:20480
	s_waitcnt lgkmcnt(5)
	v_mfma_f32_32x32x16_bf16 v[2:17], v[62:65], v[2:5], 0
	v_mfma_f32_32x32x16_bf16 v[18:33], v[62:65], v[18:21], 0
	v_mfma_f32_32x32x16_bf16 v[2:17], v[58:61], v[134:137], v[2:17]
	s_waitcnt lgkmcnt(4)
	v_mfma_f32_32x32x16_bf16 v[18:33], v[58:61], v[228:231], v[18:33]
	s_waitcnt lgkmcnt(3)
	v_mfma_f32_32x32x16_bf16 v[2:17], v[54:57], v[232:235], v[2:17]
	s_waitcnt lgkmcnt(2)
	v_mfma_f32_32x32x16_bf16 v[18:33], v[54:57], v[236:239], v[18:33]
	s_waitcnt lgkmcnt(1)
	v_mfma_f32_32x32x16_bf16 v[2:17], v[50:53], v[240:243], v[2:17]
	s_waitcnt lgkmcnt(0)
	v_mfma_f32_32x32x16_bf16 v[18:33], v[50:53], v[244:247], v[18:33]
	s_nop 9
	v_max_i32_e32 v166, 0, v2
	v_max_i32_e32 v136, 0, v10
	v_max_i32_e32 v2, 0, v3
	v_max_i32_e32 v10, 0, v11
	v_max_i32_e32 v167, 0, v18
	v_pk_fma_f32 v[134:135], v[74:75], v[166:167], 0 op_sel_hi:[1,1,0]
	v_max_i32_e32 v137, 0, v26
	v_max_i32_e32 v3, 0, v19
	v_pk_fma_f32 v[136:137], v[76:77], v[136:137], 0 op_sel_hi:[1,1,0]
	v_pk_fma_f32 v[2:3], v[46:47], v[2:3], v[134:135]
	v_max_i32_e32 v11, 0, v27
	v_max_i32_e32 v18, 0, v4
	v_max_i32_e32 v19, 0, v20
	v_pk_fma_f32 v[10:11], v[42:43], v[10:11], v[136:137]
	v_pk_fma_f32 v[2:3], v[78:79], v[18:19], v[2:3]
	v_max_i32_e32 v18, 0, v12
	v_max_i32_e32 v19, 0, v28
	v_max_i32_e32 v4, 0, v5
	v_max_i32_e32 v5, 0, v21
	v_pk_fma_f32 v[10:11], v[80:81], v[18:19], v[10:11]
	v_pk_fma_f32 v[2:3], v[48:49], v[4:5], v[2:3]
	v_max_i32_e32 v4, 0, v13
	v_max_i32_e32 v5, 0, v29
	v_pk_fma_f32 v[4:5], v[44:45], v[4:5], v[10:11]
	v_max_i32_e32 v10, 0, v6
	v_max_i32_e32 v11, 0, v22
	v_pk_fma_f32 v[2:3], v[82:83], v[10:11], v[2:3]
	v_max_i32_e32 v10, 0, v14
	v_max_i32_e32 v11, 0, v30
	v_max_i32_e32 v6, 0, v7
	v_max_i32_e32 v7, 0, v23
	v_pk_fma_f32 v[4:5], v[84:85], v[10:11], v[4:5]
	v_pk_fma_f32 v[2:3], v[38:39], v[6:7], v[2:3]
	v_max_i32_e32 v6, 0, v15
	v_max_i32_e32 v7, 0, v31
	v_pk_fma_f32 v[4:5], v[34:35], v[6:7], v[4:5]
	v_max_i32_e32 v6, 0, v8
	v_max_i32_e32 v7, 0, v24
	v_pk_fma_f32 v[2:3], v[86:87], v[6:7], v[2:3]
	v_max_i32_e32 v6, 0, v16
	v_max_i32_e32 v7, 0, v32
	v_pk_fma_f32 v[4:5], v[88:89], v[6:7], v[4:5]
	v_max_i32_e32 v6, 0, v9
	v_max_i32_e32 v7, 0, v25
	v_pk_fma_f32 v[2:3], v[40:41], v[6:7], v[2:3]
	v_max_i32_e32 v6, 0, v17
	v_max_i32_e32 v7, 0, v33
	v_pk_fma_f32 v[4:5], v[36:37], v[6:7], v[4:5]
	v_not_b32_e32 v6, v2
	v_or_b32_e32 v7, 0x80000000, v2
	v_cmp_gt_i32_e32 vcc, 0, v2
	v_not_b32_e32 v2, v3
	s_nop 0
	v_cndmask_b32_e32 v216, v7, v6, vcc
	v_or_b32_e32 v6, 0x80000000, v3
	v_cmp_gt_i32_e32 vcc, 0, v3
	v_or_b32_e32 v3, 0x80000000, v4
	s_nop 0
	v_cndmask_b32_e32 v165, v6, v2, vcc
	v_not_b32_e32 v2, v4
	v_cmp_gt_i32_e32 vcc, 0, v4
	v_permlane32_swap_b32_e32 v216, v165
	s_nop 0
	v_cndmask_b32_e32 v201, v3, v2, vcc
	v_not_b32_e32 v2, v5
	v_or_b32_e32 v3, 0x80000000, v5
	v_cmp_gt_i32_e32 vcc, 0, v5
	s_nop 1
	v_cndmask_b32_e32 v91, v3, v2, vcc
	s_nop 1
	v_permlane32_swap_b32_e32 v201, v91

.LBB0_1586:
	s_barrier
	ds_read_b128 v[2:5], v1 offset:24576
	ds_read_b128 v[18:21], v1 offset:28672
	ds_read_b128 v[134:137], v67 offset:24576
	ds_read_b128 v[228:231], v67 offset:28672
	ds_read_b128 v[232:235], v69 offset:24576
	ds_read_b128 v[236:239], v69 offset:28672
	ds_read_b128 v[240:243], v92 offset:24576
	ds_read_b128 v[244:247], v92 offset:28672
	s_waitcnt lgkmcnt(5)
	v_mfma_f32_32x32x16_bf16 v[2:17], v[62:65], v[2:5], 0
	v_mfma_f32_32x32x16_bf16 v[18:33], v[62:65], v[18:21], 0
	v_mfma_f32_32x32x16_bf16 v[2:17], v[58:61], v[134:137], v[2:17]
	s_waitcnt lgkmcnt(4)
	v_mfma_f32_32x32x16_bf16 v[18:33], v[58:61], v[228:231], v[18:33]
	s_waitcnt lgkmcnt(3)
	v_mfma_f32_32x32x16_bf16 v[2:17], v[54:57], v[232:235], v[2:17]
	s_waitcnt lgkmcnt(2)
	v_mfma_f32_32x32x16_bf16 v[18:33], v[54:57], v[236:239], v[18:33]
	s_waitcnt lgkmcnt(1)
	v_mfma_f32_32x32x16_bf16 v[2:17], v[50:53], v[240:243], v[2:17]
	s_waitcnt lgkmcnt(0)
	v_mfma_f32_32x32x16_bf16 v[18:33], v[50:53], v[244:247], v[18:33]
	s_nop 9
	v_max_i32_e32 v166, 0, v2
	v_max_i32_e32 v136, 0, v10
	v_max_i32_e32 v2, 0, v3
	v_max_i32_e32 v10, 0, v11
	v_max_i32_e32 v167, 0, v18
	v_pk_fma_f32 v[134:135], v[74:75], v[166:167], 0 op_sel_hi:[1,1,0]
	v_max_i32_e32 v137, 0, v26
	v_max_i32_e32 v3, 0, v19
	v_pk_fma_f32 v[136:137], v[76:77], v[136:137], 0 op_sel_hi:[1,1,0]
	v_pk_fma_f32 v[2:3], v[46:47], v[2:3], v[134:135]
	v_max_i32_e32 v11, 0, v27
	v_max_i32_e32 v18, 0, v4
	v_max_i32_e32 v19, 0, v20
	v_pk_fma_f32 v[10:11], v[42:43], v[10:11], v[136:137]
	v_pk_fma_f32 v[2:3], v[78:79], v[18:19], v[2:3]
	v_max_i32_e32 v18, 0, v12
	v_max_i32_e32 v19, 0, v28
	v_max_i32_e32 v4, 0, v5
	v_max_i32_e32 v5, 0, v21
	v_pk_fma_f32 v[10:11], v[80:81], v[18:19], v[10:11]
	v_pk_fma_f32 v[2:3], v[48:49], v[4:5], v[2:3]
	v_max_i32_e32 v4, 0, v13
	v_max_i32_e32 v5, 0, v29
	v_pk_fma_f32 v[4:5], v[44:45], v[4:5], v[10:11]
	v_max_i32_e32 v10, 0, v6
	v_max_i32_e32 v11, 0, v22
	v_pk_fma_f32 v[2:3], v[82:83], v[10:11], v[2:3]
	v_max_i32_e32 v10, 0, v14
	v_max_i32_e32 v11, 0, v30
	v_max_i32_e32 v6, 0, v7
	v_max_i32_e32 v7, 0, v23
	v_pk_fma_f32 v[4:5], v[84:85], v[10:11], v[4:5]
	v_pk_fma_f32 v[2:3], v[38:39], v[6:7], v[2:3]
	v_max_i32_e32 v6, 0, v15
	v_max_i32_e32 v7, 0, v31
	v_pk_fma_f32 v[4:5], v[34:35], v[6:7], v[4:5]
	v_max_i32_e32 v6, 0, v8
	v_max_i32_e32 v7, 0, v24
	v_pk_fma_f32 v[2:3], v[86:87], v[6:7], v[2:3]
	v_max_i32_e32 v6, 0, v16
	v_max_i32_e32 v7, 0, v32
	v_pk_fma_f32 v[4:5], v[88:89], v[6:7], v[4:5]
	v_max_i32_e32 v6, 0, v9
	v_max_i32_e32 v7, 0, v25
	v_pk_fma_f32 v[2:3], v[40:41], v[6:7], v[2:3]
	v_max_i32_e32 v6, 0, v17
	v_max_i32_e32 v7, 0, v33
	v_pk_fma_f32 v[4:5], v[36:37], v[6:7], v[4:5]
	v_not_b32_e32 v6, v2
	v_or_b32_e32 v7, 0x80000000, v2
	v_cmp_gt_i32_e32 vcc, 0, v2
	v_not_b32_e32 v2, v3
	s_nop 0
	v_cndmask_b32_e32 v217, v7, v6, vcc
	v_or_b32_e32 v6, 0x80000000, v3
	v_cmp_gt_i32_e32 vcc, 0, v3
	v_or_b32_e32 v3, 0x80000000, v4
	s_nop 0
	v_cndmask_b32_e32 v166, v6, v2, vcc
	v_not_b32_e32 v2, v4
	v_cmp_gt_i32_e32 vcc, 0, v4
	v_permlane32_swap_b32_e32 v217, v166
	s_nop 0
	v_cndmask_b32_e32 v202, v3, v2, vcc
	v_not_b32_e32 v2, v5
	v_or_b32_e32 v3, 0x80000000, v5
	v_cmp_gt_i32_e32 vcc, 0, v5
	s_nop 1
	v_cndmask_b32_e32 v134, v3, v2, vcc
	s_nop 1
	v_permlane32_swap_b32_e32 v202, v134

.LBB0_1599:
	s_barrier
	ds_read_b128 v[2:5], v1 offset:32768
	ds_read_b128 v[18:21], v1 offset:36864
	ds_read_b128 v[220:223], v67 offset:32768
	ds_read_b128 v[228:231], v67 offset:36864
	ds_read_b128 v[232:235], v69 offset:32768
	ds_read_b128 v[236:239], v69 offset:36864
	ds_read_b128 v[240:243], v92 offset:32768
	ds_read_b128 v[244:247], v92 offset:36864
	s_waitcnt lgkmcnt(5)
	v_mfma_f32_32x32x16_bf16 v[2:17], v[62:65], v[2:5], 0
	v_mfma_f32_32x32x16_bf16 v[18:33], v[62:65], v[18:21], 0
	v_mfma_f32_32x32x16_bf16 v[2:17], v[58:61], v[220:223], v[2:17]
	s_waitcnt lgkmcnt(4)
	v_mfma_f32_32x32x16_bf16 v[18:33], v[58:61], v[228:231], v[18:33]
	s_waitcnt lgkmcnt(3)
	v_mfma_f32_32x32x16_bf16 v[2:17], v[54:57], v[232:235], v[2:17]
	s_waitcnt lgkmcnt(2)
	v_mfma_f32_32x32x16_bf16 v[18:33], v[54:57], v[236:239], v[18:33]
	s_waitcnt lgkmcnt(1)
	v_mfma_f32_32x32x16_bf16 v[2:17], v[50:53], v[240:243], v[2:17]
	s_waitcnt lgkmcnt(0)
	v_mfma_f32_32x32x16_bf16 v[18:33], v[50:53], v[244:247], v[18:33]
	s_nop 9
	v_max_i32_e32 v136, 0, v2
	v_max_i32_e32 v168, 0, v10
	v_max_i32_e32 v2, 0, v3
	v_max_i32_e32 v10, 0, v11
	v_max_i32_e32 v137, 0, v18
	v_pk_fma_f32 v[136:137], v[74:75], v[136:137], 0 op_sel_hi:[1,1,0]
	v_max_i32_e32 v169, 0, v26
	v_max_i32_e32 v3, 0, v19
	v_pk_fma_f32 v[168:169], v[76:77], v[168:169], 0 op_sel_hi:[1,1,0]
	v_pk_fma_f32 v[2:3], v[46:47], v[2:3], v[136:137]
	v_max_i32_e32 v11, 0, v27
	v_max_i32_e32 v18, 0, v4
	v_max_i32_e32 v19, 0, v20
	v_pk_fma_f32 v[10:11], v[42:43], v[10:11], v[168:169]
	v_pk_fma_f32 v[2:3], v[78:79], v[18:19], v[2:3]
	v_max_i32_e32 v18, 0, v12
	v_max_i32_e32 v19, 0, v28
	v_max_i32_e32 v4, 0, v5
	v_max_i32_e32 v5, 0, v21
	v_pk_fma_f32 v[10:11], v[80:81], v[18:19], v[10:11]
	v_pk_fma_f32 v[2:3], v[48:49], v[4:5], v[2:3]
	v_max_i32_e32 v4, 0, v13
	v_max_i32_e32 v5, 0, v29
	v_pk_fma_f32 v[4:5], v[44:45], v[4:5], v[10:11]
	v_max_i32_e32 v10, 0, v6
	v_max_i32_e32 v11, 0, v22
	v_pk_fma_f32 v[2:3], v[82:83], v[10:11], v[2:3]
	v_max_i32_e32 v10, 0, v14
	v_max_i32_e32 v11, 0, v30
	v_max_i32_e32 v6, 0, v7
	v_max_i32_e32 v7, 0, v23
	v_pk_fma_f32 v[4:5], v[84:85], v[10:11], v[4:5]
	v_pk_fma_f32 v[2:3], v[38:39], v[6:7], v[2:3]
	v_max_i32_e32 v6, 0, v15
	v_max_i32_e32 v7, 0, v31
	v_pk_fma_f32 v[4:5], v[34:35], v[6:7], v[4:5]
	v_max_i32_e32 v6, 0, v8
	v_max_i32_e32 v7, 0, v24
	v_pk_fma_f32 v[2:3], v[86:87], v[6:7], v[2:3]
	v_max_i32_e32 v6, 0, v16
	v_max_i32_e32 v7, 0, v32
	v_pk_fma_f32 v[4:5], v[88:89], v[6:7], v[4:5]
	v_max_i32_e32 v6, 0, v9
	v_max_i32_e32 v7, 0, v25
	v_pk_fma_f32 v[2:3], v[40:41], v[6:7], v[2:3]
	v_max_i32_e32 v6, 0, v17
	v_max_i32_e32 v7, 0, v33
	v_pk_fma_f32 v[4:5], v[36:37], v[6:7], v[4:5]
	v_not_b32_e32 v6, v2
	v_or_b32_e32 v7, 0x80000000, v2
	v_cmp_gt_i32_e32 vcc, 0, v2
	v_not_b32_e32 v2, v3
	s_nop 0
	v_cndmask_b32_e32 v219, v7, v6, vcc
	v_or_b32_e32 v6, 0x80000000, v3
	v_cmp_gt_i32_e32 vcc, 0, v3
	v_or_b32_e32 v3, 0x80000000, v4
	s_nop 0
	v_cndmask_b32_e32 v167, v6, v2, vcc
	v_not_b32_e32 v2, v4
	v_cmp_gt_i32_e32 vcc, 0, v4
	v_permlane32_swap_b32_e32 v219, v167
	s_nop 0
	v_cndmask_b32_e32 v203, v3, v2, vcc
	v_not_b32_e32 v2, v5
	v_or_b32_e32 v3, 0x80000000, v5
	v_cmp_gt_i32_e32 vcc, 0, v5
	s_nop 1
	v_cndmask_b32_e32 v135, v3, v2, vcc
	s_nop 1
	v_permlane32_swap_b32_e32 v203, v135

.LBB0_1608:
	s_barrier
	ds_read_b128 v[2:5], v1 offset:40960
	ds_read_b128 v[18:21], v1 offset:45056
	ds_read_b128 v[220:223], v67 offset:40960
	ds_read_b128 v[228:231], v67 offset:45056
	ds_read_b128 v[232:235], v69 offset:40960
	ds_read_b128 v[236:239], v69 offset:45056
	ds_read_b128 v[240:243], v92 offset:40960
	ds_read_b128 v[244:247], v92 offset:45056
	s_waitcnt lgkmcnt(5)
	v_mfma_f32_32x32x16_bf16 v[2:17], v[62:65], v[2:5], 0
	v_mfma_f32_32x32x16_bf16 v[18:33], v[62:65], v[18:21], 0
	v_mfma_f32_32x32x16_bf16 v[2:17], v[58:61], v[220:223], v[2:17]
	s_waitcnt lgkmcnt(4)
	v_mfma_f32_32x32x16_bf16 v[18:33], v[58:61], v[228:231], v[18:33]
	s_waitcnt lgkmcnt(3)
	v_mfma_f32_32x32x16_bf16 v[2:17], v[54:57], v[232:235], v[2:17]
	s_waitcnt lgkmcnt(2)
	v_mfma_f32_32x32x16_bf16 v[18:33], v[54:57], v[236:239], v[18:33]
	s_waitcnt lgkmcnt(1)
	v_mfma_f32_32x32x16_bf16 v[2:17], v[50:53], v[240:243], v[2:17]
	s_waitcnt lgkmcnt(0)
	v_mfma_f32_32x32x16_bf16 v[18:33], v[50:53], v[244:247], v[18:33]
	s_nop 9
	v_max_i32_e32 v136, 0, v2
	v_max_i32_e32 v168, 0, v10
	v_max_i32_e32 v2, 0, v3
	v_max_i32_e32 v10, 0, v11
	v_max_i32_e32 v137, 0, v18
	v_pk_fma_f32 v[136:137], v[74:75], v[136:137], 0 op_sel_hi:[1,1,0]
	v_max_i32_e32 v169, 0, v26
	v_max_i32_e32 v3, 0, v19
	v_pk_fma_f32 v[168:169], v[76:77], v[168:169], 0 op_sel_hi:[1,1,0]
	v_pk_fma_f32 v[2:3], v[46:47], v[2:3], v[136:137]
	v_max_i32_e32 v11, 0, v27
	v_max_i32_e32 v18, 0, v4
	v_max_i32_e32 v19, 0, v20
	v_pk_fma_f32 v[10:11], v[42:43], v[10:11], v[168:169]
	v_pk_fma_f32 v[2:3], v[78:79], v[18:19], v[2:3]
	v_max_i32_e32 v18, 0, v12
	v_max_i32_e32 v19, 0, v28
	v_max_i32_e32 v4, 0, v5
	v_max_i32_e32 v5, 0, v21
	v_pk_fma_f32 v[10:11], v[80:81], v[18:19], v[10:11]
	v_pk_fma_f32 v[2:3], v[48:49], v[4:5], v[2:3]
	v_max_i32_e32 v4, 0, v13
	v_max_i32_e32 v5, 0, v29
	v_pk_fma_f32 v[4:5], v[44:45], v[4:5], v[10:11]
	v_max_i32_e32 v10, 0, v6
	v_max_i32_e32 v11, 0, v22
	v_pk_fma_f32 v[2:3], v[82:83], v[10:11], v[2:3]
	v_max_i32_e32 v10, 0, v14
	v_max_i32_e32 v11, 0, v30
	v_max_i32_e32 v6, 0, v7
	v_max_i32_e32 v7, 0, v23
	v_pk_fma_f32 v[4:5], v[84:85], v[10:11], v[4:5]
	v_pk_fma_f32 v[2:3], v[38:39], v[6:7], v[2:3]
	v_max_i32_e32 v6, 0, v15
	v_max_i32_e32 v7, 0, v31
	v_pk_fma_f32 v[4:5], v[34:35], v[6:7], v[4:5]
	v_max_i32_e32 v6, 0, v8
	v_max_i32_e32 v7, 0, v24
	v_pk_fma_f32 v[2:3], v[86:87], v[6:7], v[2:3]
	v_max_i32_e32 v6, 0, v16
	v_max_i32_e32 v7, 0, v32
	v_pk_fma_f32 v[4:5], v[88:89], v[6:7], v[4:5]
	v_max_i32_e32 v6, 0, v9
	v_max_i32_e32 v7, 0, v25
	v_pk_fma_f32 v[2:3], v[40:41], v[6:7], v[2:3]
	v_max_i32_e32 v6, 0, v17
	v_max_i32_e32 v7, 0, v33
	v_pk_fma_f32 v[4:5], v[36:37], v[6:7], v[4:5]
	v_not_b32_e32 v6, v2
	v_or_b32_e32 v7, 0x80000000, v2
	v_cmp_gt_i32_e32 vcc, 0, v2
	v_not_b32_e32 v2, v3
	s_nop 0
	v_cndmask_b32_e32 v220, v7, v6, vcc
	v_or_b32_e32 v6, 0x80000000, v3
	v_cmp_gt_i32_e32 vcc, 0, v3
	v_or_b32_e32 v3, 0x80000000, v4
	s_nop 0
	v_cndmask_b32_e32 v168, v6, v2, vcc
	v_not_b32_e32 v2, v4
	v_cmp_gt_i32_e32 vcc, 0, v4
	v_permlane32_swap_b32_e32 v220, v168
	s_nop 0
	v_cndmask_b32_e32 v204, v3, v2, vcc
	v_not_b32_e32 v2, v5
	v_or_b32_e32 v3, 0x80000000, v5
	v_cmp_gt_i32_e32 vcc, 0, v5
	s_nop 1
	v_cndmask_b32_e32 v136, v3, v2, vcc
	s_nop 1
	v_permlane32_swap_b32_e32 v204, v136

.LBB0_1614:
	s_barrier
	ds_read_b128 v[2:5], v1 offset:49152
	ds_read_b128 v[18:21], v1 offset:53248
	ds_read_b128 v[222:225], v67 offset:49152
	ds_read_b128 v[228:231], v67 offset:53248
	ds_read_b128 v[232:235], v69 offset:49152
	ds_read_b128 v[236:239], v69 offset:53248
	ds_read_b128 v[240:243], v92 offset:49152
	ds_read_b128 v[244:247], v92 offset:53248
	s_waitcnt lgkmcnt(5)
	v_mfma_f32_32x32x16_bf16 v[2:17], v[62:65], v[2:5], 0
	v_mfma_f32_32x32x16_bf16 v[18:33], v[62:65], v[18:21], 0
	v_mfma_f32_32x32x16_bf16 v[2:17], v[58:61], v[222:225], v[2:17]
	s_waitcnt lgkmcnt(4)
	v_mfma_f32_32x32x16_bf16 v[18:33], v[58:61], v[228:231], v[18:33]
	s_waitcnt lgkmcnt(3)
	v_mfma_f32_32x32x16_bf16 v[2:17], v[54:57], v[232:235], v[2:17]
	s_waitcnt lgkmcnt(2)
	v_mfma_f32_32x32x16_bf16 v[18:33], v[54:57], v[236:239], v[18:33]
	s_waitcnt lgkmcnt(1)
	v_mfma_f32_32x32x16_bf16 v[2:17], v[50:53], v[240:243], v[2:17]
	s_waitcnt lgkmcnt(0)
	v_mfma_f32_32x32x16_bf16 v[18:33], v[50:53], v[244:247], v[18:33]
	s_nop 9
	v_max_i32_e32 v226, 0, v2
	v_max_i32_e32 v224, 0, v10
	v_max_i32_e32 v2, 0, v3
	v_max_i32_e32 v10, 0, v11
	v_max_i32_e32 v227, 0, v18
	v_pk_fma_f32 v[222:223], v[74:75], v[226:227], 0 op_sel_hi:[1,1,0]
	v_max_i32_e32 v225, 0, v26
	v_max_i32_e32 v3, 0, v19
	v_pk_fma_f32 v[224:225], v[76:77], v[224:225], 0 op_sel_hi:[1,1,0]
	v_pk_fma_f32 v[2:3], v[46:47], v[2:3], v[222:223]
	v_max_i32_e32 v11, 0, v27
	v_max_i32_e32 v18, 0, v4
	v_max_i32_e32 v19, 0, v20
	v_pk_fma_f32 v[10:11], v[42:43], v[10:11], v[224:225]
	v_pk_fma_f32 v[2:3], v[78:79], v[18:19], v[2:3]
	v_max_i32_e32 v18, 0, v12
	v_max_i32_e32 v19, 0, v28
	v_max_i32_e32 v4, 0, v5
	v_max_i32_e32 v5, 0, v21
	v_pk_fma_f32 v[10:11], v[80:81], v[18:19], v[10:11]
	v_pk_fma_f32 v[2:3], v[48:49], v[4:5], v[2:3]
	v_max_i32_e32 v4, 0, v13
	v_max_i32_e32 v5, 0, v29
	v_pk_fma_f32 v[4:5], v[44:45], v[4:5], v[10:11]
	v_max_i32_e32 v10, 0, v6
	v_max_i32_e32 v11, 0, v22
	v_pk_fma_f32 v[2:3], v[82:83], v[10:11], v[2:3]
	v_max_i32_e32 v10, 0, v14
	v_max_i32_e32 v11, 0, v30
	v_max_i32_e32 v6, 0, v7
	v_max_i32_e32 v7, 0, v23
	v_pk_fma_f32 v[4:5], v[84:85], v[10:11], v[4:5]
	v_pk_fma_f32 v[2:3], v[38:39], v[6:7], v[2:3]
	v_max_i32_e32 v6, 0, v15
	v_max_i32_e32 v7, 0, v31
	v_pk_fma_f32 v[4:5], v[34:35], v[6:7], v[4:5]
	v_max_i32_e32 v6, 0, v8
	v_max_i32_e32 v7, 0, v24
	v_pk_fma_f32 v[2:3], v[86:87], v[6:7], v[2:3]
	v_max_i32_e32 v6, 0, v16
	v_max_i32_e32 v7, 0, v32
	v_pk_fma_f32 v[4:5], v[88:89], v[6:7], v[4:5]
	v_max_i32_e32 v6, 0, v9
	v_max_i32_e32 v7, 0, v25
	v_pk_fma_f32 v[2:3], v[40:41], v[6:7], v[2:3]
	v_max_i32_e32 v6, 0, v17
	v_max_i32_e32 v7, 0, v33
	v_pk_fma_f32 v[4:5], v[36:37], v[6:7], v[4:5]
	v_not_b32_e32 v6, v2
	v_or_b32_e32 v7, 0x80000000, v2
	v_cmp_gt_i32_e32 vcc, 0, v2
	v_not_b32_e32 v2, v3
	s_nop 0
	v_cndmask_b32_e32 v221, v7, v6, vcc
	v_or_b32_e32 v6, 0x80000000, v3
	v_cmp_gt_i32_e32 vcc, 0, v3
	v_or_b32_e32 v3, 0x80000000, v4
	s_nop 0
	v_cndmask_b32_e32 v169, v6, v2, vcc
	v_not_b32_e32 v2, v4
	v_cmp_gt_i32_e32 vcc, 0, v4
	v_permlane32_swap_b32_e32 v221, v169
	s_nop 0
	v_cndmask_b32_e32 v205, v3, v2, vcc
	v_not_b32_e32 v2, v5
	v_or_b32_e32 v3, 0x80000000, v5
	v_cmp_gt_i32_e32 vcc, 0, v5
	s_nop 1
	v_cndmask_b32_e32 v137, v3, v2, vcc
	s_nop 1
	v_permlane32_swap_b32_e32 v205, v137
